# kloop_redundant_lgkmcnt0_before_mfma_removed
# baseline (speedup 1.0000x reference)
.LBB0_253:
	v_add_u32_e32 v133, 0x10000, v131
	ds_read_b128 v[136:139], v133
	ds_read_b128 v[140:143], v133 offset:1024
	ds_read_b128 v[144:147], v133 offset:2048
	ds_read_b128 v[148:151], v133 offset:3072
	v_add_u32_e32 v133, 0x14000, v131
	ds_read_b128 v[152:155], v133
	ds_read_b128 v[156:159], v133 offset:1024
	ds_read_b128 v[160:163], v133 offset:2048
	ds_read_b128 v[164:167], v133 offset:3072
	s_cmp_eq_u32 s25, s61
	s_cselect_b64 s[66:67], -1, 0
	v_lshl_add_u64 v[192:193], s[0:1], 0, v[194:195]
	s_mov_b32 m0, s56
	v_lshl_add_u64 v[192:193], v[192:193], 0, s[26:27]
	v_mov_b32_e32 v133, v195
	ds_read_b128 v[168:171], v135
	ds_read_b128 v[172:175], v135 offset:1024
	ds_read_b128 v[176:179], v135 offset:2048
	ds_read_b128 v[180:183], v135 offset:3072
	ds_read_b128 v[184:187], v135 offset:4096
	ds_read_b128 v[188:191], v135 offset:5120
	ds_read_b128 v[196:199], v135 offset:6144
	ds_read_b128 v[200:203], v135 offset:7168
	global_load_lds_dwordx4 v[192:193], off
	v_lshl_add_u64 v[192:193], s[0:1], 0, v[132:133]
	v_lshl_add_u64 v[192:193], v[192:193], 0, s[26:27]
	s_mov_b32 m0, s57
	s_nop 0
	global_load_lds_dwordx4 v[192:193], off
	s_cmp_lg_u32 s100, 0
	s_waitcnt vmcnt(8)
	s_waitcnt lgkmcnt(0)
	s_barrier
	s_setprio 1
	s_cbranch_scc1 .Lcz1_253
	v_mfma_f32_16x16x32_bf16 v[126:129], v[136:139], v[168:171], v[126:129]
	v_mfma_f32_16x16x32_bf16 v[122:125], v[144:147], v[168:171], v[122:125]
	v_mfma_f32_16x16x32_bf16 v[114:117], v[136:139], v[176:179], v[114:117]
	v_mfma_f32_16x16x32_bf16 v[110:113], v[144:147], v[176:179], v[110:113]
	v_mfma_f32_16x16x32_bf16 v[94:97], v[136:139], v[184:187], v[94:97]
	v_mfma_f32_16x16x32_bf16 v[90:93], v[144:147], v[184:187], v[90:93]
	v_mfma_f32_16x16x32_bf16 v[78:81], v[136:139], v[196:199], v[78:81]
	v_mfma_f32_16x16x32_bf16 v[74:77], v[144:147], v[196:199], v[74:77]
	v_mfma_f32_16x16x32_bf16 v[126:129], v[140:143], v[172:175], v[126:129]
	v_mfma_f32_16x16x32_bf16 v[122:125], v[148:151], v[172:175], v[122:125]
	v_mfma_f32_16x16x32_bf16 v[114:117], v[140:143], v[180:183], v[114:117]
	v_mfma_f32_16x16x32_bf16 v[110:113], v[148:151], v[180:183], v[110:113]
	v_mfma_f32_16x16x32_bf16 v[94:97], v[140:143], v[188:191], v[94:97]
	v_mfma_f32_16x16x32_bf16 v[90:93], v[148:151], v[188:191], v[90:93]
	v_mfma_f32_16x16x32_bf16 v[78:81], v[140:143], v[200:203], v[78:81]
	v_mfma_f32_16x16x32_bf16 v[74:77], v[148:151], v[200:203], v[74:77]
	s_setprio 0
	s_setprio 1
	v_mfma_f32_16x16x32_bf16 v[106:109], v[152:155], v[168:171], v[106:109]
	v_mfma_f32_16x16x32_bf16 v[118:121], v[160:163], v[168:171], v[118:121]
	v_mfma_f32_16x16x32_bf16 v[102:105], v[152:155], v[176:179], v[102:105]
	v_mfma_f32_16x16x32_bf16 v[98:101], v[160:163], v[176:179], v[98:101]
	v_mfma_f32_16x16x32_bf16 v[86:89], v[152:155], v[184:187], v[86:89]
	v_mfma_f32_16x16x32_bf16 v[82:85], v[160:163], v[184:187], v[82:85]
	v_mfma_f32_16x16x32_bf16 v[70:73], v[152:155], v[196:199], v[70:73]
	v_mfma_f32_16x16x32_bf16 v[66:69], v[160:163], v[196:199], v[66:69]
	v_mfma_f32_16x16x32_bf16 v[106:109], v[156:159], v[172:175], v[106:109]
	v_mfma_f32_16x16x32_bf16 v[118:121], v[164:167], v[172:175], v[118:121]
	v_mfma_f32_16x16x32_bf16 v[102:105], v[156:159], v[180:183], v[102:105]
	v_mfma_f32_16x16x32_bf16 v[98:101], v[164:167], v[180:183], v[98:101]
	v_mfma_f32_16x16x32_bf16 v[86:89], v[156:159], v[188:191], v[86:89]
	v_mfma_f32_16x16x32_bf16 v[82:85], v[164:167], v[188:191], v[82:85]
	v_mfma_f32_16x16x32_bf16 v[70:73], v[156:159], v[200:203], v[70:73]
	v_mfma_f32_16x16x32_bf16 v[66:69], v[164:167], v[200:203], v[66:69]
.Lcj1_253:
	s_setprio 0
	s_barrier
	s_and_b64 s[68:69], s[66:67], exec
	s_cselect_b32 s62, 0, s61
	s_and_b64 s[66:67], s[2:3], s[66:67]
	s_and_b64 s[66:67], s[66:67], exec
	s_cselect_b32 s5, s60, s5
	s_cselect_b32 s4, s21, s4
	s_cselect_b32 s1, s59, s1
	s_cselect_b32 s0, s23, s0
	s_lshl_b64 s[66:67], s[62:63], 7
	s_add_u32 s68, s4, s66
	s_addc_u32 s69, s5, s67
	s_mov_b32 m0, s41
	s_add_u32 s72, s4, 0x40000
	ds_read_b128 v[168:171], v135 offset:16384
	ds_read_b128 v[172:175], v135 offset:17408
	ds_read_b128 v[176:179], v135 offset:18432
	ds_read_b128 v[180:183], v135 offset:19456
	ds_read_b128 v[184:187], v135 offset:20480
	ds_read_b128 v[188:191], v135 offset:21504
	ds_read_b128 v[196:199], v135 offset:22528
	ds_read_b128 v[200:203], v135 offset:23552
	global_load_lds_dwordx4 v130, s[68:69]
	s_mov_b32 m0, s42
	s_addc_u32 s73, s5, 0
	global_load_lds_dwordx4 v134, s[68:69]
	s_add_u32 s68, s72, s66
	s_addc_u32 s69, s73, s67
	s_mov_b32 m0, s43
	s_add_u32 s66, s0, s66
	global_load_lds_dwordx4 v130, s[68:69]
	s_mov_b32 m0, s44
	s_addc_u32 s67, s1, s67
	global_load_lds_dwordx4 v134, s[68:69]
	s_mov_b32 m0, s40
	s_nop 0
	global_load_lds_dwordx4 v194, s[66:67]
	s_mov_b32 m0, s45
	s_nop 0
	global_load_lds_dwordx4 v132, s[66:67]
	s_cmp_lg_u32 s100, 0
	s_waitcnt vmcnt(8)
	s_waitcnt lgkmcnt(0)
	s_barrier
	s_setprio 1
	s_cbranch_scc1 .Lcz2_253
	v_mfma_f32_16x16x32_bf16 v[62:65], v[136:139], v[168:171], v[62:65]
	v_mfma_f32_16x16x32_bf16 v[58:61], v[144:147], v[168:171], v[58:61]
	v_mfma_f32_16x16x32_bf16 v[46:49], v[136:139], v[176:179], v[46:49]
	v_mfma_f32_16x16x32_bf16 v[42:45], v[144:147], v[176:179], v[42:45]
	v_mfma_f32_16x16x32_bf16 v[30:33], v[136:139], v[184:187], v[30:33]
	v_mfma_f32_16x16x32_bf16 v[26:29], v[144:147], v[184:187], v[26:29]
	v_mfma_f32_16x16x32_bf16 v[14:17], v[136:139], v[196:199], v[14:17]
	v_mfma_f32_16x16x32_bf16 v[10:13], v[144:147], v[196:199], v[10:13]
	v_mfma_f32_16x16x32_bf16 v[62:65], v[140:143], v[172:175], v[62:65]
	v_mfma_f32_16x16x32_bf16 v[58:61], v[148:151], v[172:175], v[58:61]
	v_mfma_f32_16x16x32_bf16 v[46:49], v[140:143], v[180:183], v[46:49]
	v_mfma_f32_16x16x32_bf16 v[42:45], v[148:151], v[180:183], v[42:45]
	v_mfma_f32_16x16x32_bf16 v[30:33], v[140:143], v[188:191], v[30:33]
	v_mfma_f32_16x16x32_bf16 v[26:29], v[148:151], v[188:191], v[26:29]
	v_mfma_f32_16x16x32_bf16 v[14:17], v[140:143], v[200:203], v[14:17]
	v_mfma_f32_16x16x32_bf16 v[10:13], v[148:151], v[200:203], v[10:13]
	s_setprio 0
	s_setprio 1
	v_mfma_f32_16x16x32_bf16 v[54:57], v[152:155], v[168:171], v[54:57]
	v_mfma_f32_16x16x32_bf16 v[50:53], v[160:163], v[168:171], v[50:53]
	v_mfma_f32_16x16x32_bf16 v[38:41], v[152:155], v[176:179], v[38:41]
	v_mfma_f32_16x16x32_bf16 v[34:37], v[160:163], v[176:179], v[34:37]
	v_mfma_f32_16x16x32_bf16 v[22:25], v[152:155], v[184:187], v[22:25]
	v_mfma_f32_16x16x32_bf16 v[18:21], v[160:163], v[184:187], v[18:21]
	v_mfma_f32_16x16x32_bf16 v[6:9], v[152:155], v[196:199], v[6:9]
	v_mfma_f32_16x16x32_bf16 v[2:5], v[160:163], v[196:199], v[2:5]
	v_mfma_f32_16x16x32_bf16 v[54:57], v[156:159], v[172:175], v[54:57]
	v_mfma_f32_16x16x32_bf16 v[50:53], v[164:167], v[172:175], v[50:53]
	v_mfma_f32_16x16x32_bf16 v[38:41], v[156:159], v[180:183], v[38:41]
	v_mfma_f32_16x16x32_bf16 v[34:37], v[164:167], v[180:183], v[34:37]
	v_mfma_f32_16x16x32_bf16 v[22:25], v[156:159], v[188:191], v[22:25]
	v_mfma_f32_16x16x32_bf16 v[18:21], v[164:167], v[188:191], v[18:21]
	v_mfma_f32_16x16x32_bf16 v[6:9], v[156:159], v[200:203], v[6:9]
	v_mfma_f32_16x16x32_bf16 v[2:5], v[164:167], v[200:203], v[2:5]
.Lcj2_253:
	s_setprio 0
	s_barrier
	v_add_u32_e32 v133, 0x18000, v131
	ds_read_b128 v[136:139], v133
	ds_read_b128 v[140:143], v133 offset:1024
	ds_read_b128 v[144:147], v133 offset:2048
	ds_read_b128 v[148:151], v133 offset:3072
	v_add_u32_e32 v133, 0x1c000, v131
	ds_read_b128 v[152:155], v133
	ds_read_b128 v[156:159], v133 offset:1024
	ds_read_b128 v[160:163], v133 offset:2048
	ds_read_b128 v[164:167], v133 offset:3072
	s_add_u32 s66, s66, 0x40000
	s_addc_u32 s67, s67, 0
	s_mov_b32 m0, s46
	ds_read_b128 v[168:171], v135 offset:32768
	ds_read_b128 v[172:175], v135 offset:33792
	ds_read_b128 v[176:179], v135 offset:34816
	ds_read_b128 v[180:183], v135 offset:35840
	ds_read_b128 v[184:187], v135 offset:36864
	ds_read_b128 v[188:191], v135 offset:37888
	ds_read_b128 v[196:199], v135 offset:38912
	ds_read_b128 v[200:203], v135 offset:39936
	global_load_lds_dwordx4 v194, s[66:67]
	s_mov_b32 m0, s47
	s_nop 0
	global_load_lds_dwordx4 v132, s[66:67]
	s_waitcnt vmcnt(8)
	s_waitcnt lgkmcnt(0)
	s_barrier
	s_setprio 1
	v_mfma_f32_16x16x32_bf16 v[126:129], v[136:139], v[168:171], v[126:129]
	v_mfma_f32_16x16x32_bf16 v[122:125], v[144:147], v[168:171], v[122:125]
	v_mfma_f32_16x16x32_bf16 v[114:117], v[136:139], v[176:179], v[114:117]
	v_mfma_f32_16x16x32_bf16 v[110:113], v[144:147], v[176:179], v[110:113]
	v_mfma_f32_16x16x32_bf16 v[94:97], v[136:139], v[184:187], v[94:97]
	v_mfma_f32_16x16x32_bf16 v[90:93], v[144:147], v[184:187], v[90:93]
	v_mfma_f32_16x16x32_bf16 v[78:81], v[136:139], v[196:199], v[78:81]
	v_mfma_f32_16x16x32_bf16 v[74:77], v[144:147], v[196:199], v[74:77]
	v_mfma_f32_16x16x32_bf16 v[126:129], v[140:143], v[172:175], v[126:129]
	v_mfma_f32_16x16x32_bf16 v[122:125], v[148:151], v[172:175], v[122:125]
	v_mfma_f32_16x16x32_bf16 v[114:117], v[140:143], v[180:183], v[114:117]
	v_mfma_f32_16x16x32_bf16 v[110:113], v[148:151], v[180:183], v[110:113]
	v_mfma_f32_16x16x32_bf16 v[94:97], v[140:143], v[188:191], v[94:97]
	v_mfma_f32_16x16x32_bf16 v[90:93], v[148:151], v[188:191], v[90:93]
	v_mfma_f32_16x16x32_bf16 v[78:81], v[140:143], v[200:203], v[78:81]
	v_mfma_f32_16x16x32_bf16 v[74:77], v[148:151], v[200:203], v[74:77]
	s_setprio 0
	s_setprio 1
	v_mfma_f32_16x16x32_bf16 v[106:109], v[152:155], v[168:171], v[106:109]
	v_mfma_f32_16x16x32_bf16 v[118:121], v[160:163], v[168:171], v[118:121]
	v_mfma_f32_16x16x32_bf16 v[102:105], v[152:155], v[176:179], v[102:105]
	v_mfma_f32_16x16x32_bf16 v[98:101], v[160:163], v[176:179], v[98:101]
	v_mfma_f32_16x16x32_bf16 v[86:89], v[152:155], v[184:187], v[86:89]
	v_mfma_f32_16x16x32_bf16 v[82:85], v[160:163], v[184:187], v[82:85]
	v_mfma_f32_16x16x32_bf16 v[70:73], v[152:155], v[196:199], v[70:73]
	v_mfma_f32_16x16x32_bf16 v[66:69], v[160:163], v[196:199], v[66:69]
	v_mfma_f32_16x16x32_bf16 v[106:109], v[156:159], v[172:175], v[106:109]
	v_mfma_f32_16x16x32_bf16 v[118:121], v[164:167], v[172:175], v[118:121]
	v_mfma_f32_16x16x32_bf16 v[102:105], v[156:159], v[180:183], v[102:105]
	v_mfma_f32_16x16x32_bf16 v[98:101], v[164:167], v[180:183], v[98:101]
	v_mfma_f32_16x16x32_bf16 v[86:89], v[156:159], v[188:191], v[86:89]
	v_mfma_f32_16x16x32_bf16 v[82:85], v[164:167], v[188:191], v[82:85]
	v_mfma_f32_16x16x32_bf16 v[70:73], v[156:159], v[200:203], v[70:73]
	v_mfma_f32_16x16x32_bf16 v[66:69], v[164:167], v[200:203], v[66:69]
	s_setprio 0
	s_barrier
	s_or_b32 s62, s62, 1
	s_lshl_b64 s[66:67], s[62:63], 7
	s_add_u32 s68, s4, s66
	s_mov_b32 m0, s48
	s_addc_u32 s69, s5, s67
	ds_read_b128 v[168:171], v135 offset:49152
	ds_read_b128 v[172:175], v135 offset:50176
	ds_read_b128 v[176:179], v135 offset:51200
	ds_read_b128 v[180:183], v135 offset:52224
	ds_read_b128 v[184:187], v135 offset:53248
	ds_read_b128 v[188:191], v135 offset:54272
	ds_read_b128 v[196:199], v135 offset:55296
	ds_read_b128 v[200:203], v135 offset:56320
	global_load_lds_dwordx4 v130, s[68:69]
	s_mov_b32 m0, s49
	s_nop 0
	global_load_lds_dwordx4 v134, s[68:69]
	s_add_u32 s68, s72, s66
	s_addc_u32 s69, s73, s67
	s_mov_b32 m0, s52
	s_add_u32 s66, s0, s66
	global_load_lds_dwordx4 v130, s[68:69]
	s_mov_b32 m0, s53
	s_addc_u32 s67, s1, s67
	global_load_lds_dwordx4 v134, s[68:69]
	s_mov_b32 m0, s50
	s_nop 0
	global_load_lds_dwordx4 v194, s[66:67]
	s_mov_b32 m0, s51
	s_nop 0
	global_load_lds_dwordx4 v132, s[66:67]
	s_waitcnt vmcnt(8)
	s_waitcnt lgkmcnt(0)
	s_barrier
	s_setprio 1
	v_mfma_f32_16x16x32_bf16 v[62:65], v[136:139], v[168:171], v[62:65]
	v_mfma_f32_16x16x32_bf16 v[58:61], v[144:147], v[168:171], v[58:61]
	v_mfma_f32_16x16x32_bf16 v[46:49], v[136:139], v[176:179], v[46:49]
	v_mfma_f32_16x16x32_bf16 v[42:45], v[144:147], v[176:179], v[42:45]
	v_mfma_f32_16x16x32_bf16 v[30:33], v[136:139], v[184:187], v[30:33]
	v_mfma_f32_16x16x32_bf16 v[26:29], v[144:147], v[184:187], v[26:29]
	v_mfma_f32_16x16x32_bf16 v[14:17], v[136:139], v[196:199], v[14:17]
	v_mfma_f32_16x16x32_bf16 v[10:13], v[144:147], v[196:199], v[10:13]
	v_mfma_f32_16x16x32_bf16 v[62:65], v[140:143], v[172:175], v[62:65]
	v_mfma_f32_16x16x32_bf16 v[58:61], v[148:151], v[172:175], v[58:61]
	v_mfma_f32_16x16x32_bf16 v[46:49], v[140:143], v[180:183], v[46:49]
	v_mfma_f32_16x16x32_bf16 v[42:45], v[148:151], v[180:183], v[42:45]
	v_mfma_f32_16x16x32_bf16 v[30:33], v[140:143], v[188:191], v[30:33]
	v_mfma_f32_16x16x32_bf16 v[26:29], v[148:151], v[188:191], v[26:29]
	v_mfma_f32_16x16x32_bf16 v[14:17], v[140:143], v[200:203], v[14:17]
	v_mfma_f32_16x16x32_bf16 v[10:13], v[148:151], v[200:203], v[10:13]
	s_setprio 0
	s_setprio 1
	v_mfma_f32_16x16x32_bf16 v[54:57], v[152:155], v[168:171], v[54:57]
	v_mfma_f32_16x16x32_bf16 v[50:53], v[160:163], v[168:171], v[50:53]
	v_mfma_f32_16x16x32_bf16 v[38:41], v[152:155], v[176:179], v[38:41]
	v_mfma_f32_16x16x32_bf16 v[34:37], v[160:163], v[176:179], v[34:37]
	v_mfma_f32_16x16x32_bf16 v[22:25], v[152:155], v[184:187], v[22:25]
	v_mfma_f32_16x16x32_bf16 v[18:21], v[160:163], v[184:187], v[18:21]
	v_mfma_f32_16x16x32_bf16 v[6:9], v[152:155], v[196:199], v[6:9]
	v_mfma_f32_16x16x32_bf16 v[2:5], v[160:163], v[196:199], v[2:5]
	v_mfma_f32_16x16x32_bf16 v[54:57], v[156:159], v[172:175], v[54:57]
	v_mfma_f32_16x16x32_bf16 v[50:53], v[164:167], v[172:175], v[50:53]
	v_mfma_f32_16x16x32_bf16 v[38:41], v[156:159], v[180:183], v[38:41]
	v_mfma_f32_16x16x32_bf16 v[34:37], v[164:167], v[180:183], v[34:37]
	v_mfma_f32_16x16x32_bf16 v[22:25], v[156:159], v[188:191], v[22:25]
	v_mfma_f32_16x16x32_bf16 v[18:21], v[164:167], v[188:191], v[18:21]
	v_mfma_f32_16x16x32_bf16 v[6:9], v[156:159], v[200:203], v[6:9]
	v_mfma_f32_16x16x32_bf16 v[2:5], v[164:167], v[200:203], v[2:5]
	s_setprio 0
	s_barrier
	s_add_i32 s62, s61, 2
	s_add_u32 s26, s26, 0x100
	s_addc_u32 s27, s27, 0
	s_cmp_ge_i32 s61, s25
	s_mov_b32 s61, s62
	s_cbranch_scc0 .LBB0_253
	s_branch .Lcsk_253

.LBB0_287:
	v_add_u32_e32 v130, 0x10000, v165
	v_add_u32_e32 v142, 0x14000, v165
	ds_read_b128 v[146:149], v130
	ds_read_b128 v[150:153], v130 offset:1024
	ds_read_b128 v[154:157], v130 offset:2048
	ds_read_b128 v[158:161], v130 offset:3072
	ds_read_b128 v[130:133], v142
	ds_read_b128 v[134:137], v142 offset:1024
	ds_read_b128 v[138:141], v142 offset:2048
	ds_read_b128 v[142:145], v142 offset:3072
	s_add_i32 m0, s13, 0xc000
	s_add_i32 s26, s13, 0xe000
	s_cmp_lg_u32 s55, s56
	s_cselect_b64 s[58:59], -1, 0
	v_lshl_add_u64 v[204:205], s[10:11], 0, v[194:195]
	v_lshl_add_u64 v[204:205], v[204:205], 0, s[24:25]
	v_mov_b32_e32 v163, v195
	ds_read_b128 v[174:177], v167
	ds_read_b128 v[178:181], v167 offset:1024
	ds_read_b128 v[182:185], v167 offset:2048
	ds_read_b128 v[186:189], v167 offset:3072
	ds_read_b128 v[190:193], v167 offset:4096
	ds_read_b128 v[196:199], v167 offset:5120
	ds_read_b128 v[200:203], v167 offset:6144
	ds_read_b128 v[216:219], v167 offset:7168
	global_load_lds_dwordx4 v[204:205], off
	v_lshl_add_u64 v[204:205], s[10:11], 0, v[162:163]
	v_lshl_add_u64 v[204:205], v[204:205], 0, s[24:25]
	s_mov_b32 m0, s26
	s_nop 0
	global_load_lds_dwordx4 v[204:205], off
	s_cmp_lg_u32 s100, 0
	s_waitcnt vmcnt(8)
	s_waitcnt lgkmcnt(0)
	s_barrier
	s_setprio 1
	s_cbranch_scc1 .Lcz1_287
	v_mfma_f32_16x16x32_bf16 v[126:129], v[146:149], v[174:177], v[126:129]
	v_mfma_f32_16x16x32_bf16 v[122:125], v[154:157], v[174:177], v[122:125]
	v_mfma_f32_16x16x32_bf16 v[110:113], v[146:149], v[182:185], v[110:113]
	v_mfma_f32_16x16x32_bf16 v[106:109], v[154:157], v[182:185], v[106:109]
	v_mfma_f32_16x16x32_bf16 v[94:97], v[146:149], v[190:193], v[94:97]
	v_mfma_f32_16x16x32_bf16 v[90:93], v[154:157], v[190:193], v[90:93]
	v_mfma_f32_16x16x32_bf16 v[78:81], v[146:149], v[200:203], v[78:81]
	v_mfma_f32_16x16x32_bf16 v[74:77], v[154:157], v[200:203], v[74:77]
	v_mfma_f32_16x16x32_bf16 v[126:129], v[150:153], v[178:181], v[126:129]
	v_mfma_f32_16x16x32_bf16 v[122:125], v[158:161], v[178:181], v[122:125]
	v_mfma_f32_16x16x32_bf16 v[110:113], v[150:153], v[186:189], v[110:113]
	v_mfma_f32_16x16x32_bf16 v[106:109], v[158:161], v[186:189], v[106:109]
	v_mfma_f32_16x16x32_bf16 v[94:97], v[150:153], v[196:199], v[94:97]
	v_mfma_f32_16x16x32_bf16 v[90:93], v[158:161], v[196:199], v[90:93]
	v_mfma_f32_16x16x32_bf16 v[78:81], v[150:153], v[216:219], v[78:81]
	v_mfma_f32_16x16x32_bf16 v[74:77], v[158:161], v[216:219], v[74:77]
	s_setprio 0
	s_setprio 1
	v_mfma_f32_16x16x32_bf16 v[118:121], v[130:133], v[174:177], v[118:121]
	v_mfma_f32_16x16x32_bf16 v[114:117], v[138:141], v[174:177], v[114:117]
	v_mfma_f32_16x16x32_bf16 v[102:105], v[130:133], v[182:185], v[102:105]
	v_mfma_f32_16x16x32_bf16 v[98:101], v[138:141], v[182:185], v[98:101]
	v_mfma_f32_16x16x32_bf16 v[86:89], v[130:133], v[190:193], v[86:89]
	v_mfma_f32_16x16x32_bf16 v[82:85], v[138:141], v[190:193], v[82:85]
	v_mfma_f32_16x16x32_bf16 v[70:73], v[130:133], v[200:203], v[70:73]
	v_mfma_f32_16x16x32_bf16 v[66:69], v[138:141], v[200:203], v[66:69]
	v_mfma_f32_16x16x32_bf16 v[118:121], v[134:137], v[178:181], v[118:121]
	v_mfma_f32_16x16x32_bf16 v[114:117], v[142:145], v[178:181], v[114:117]
	v_mfma_f32_16x16x32_bf16 v[102:105], v[134:137], v[186:189], v[102:105]
	v_mfma_f32_16x16x32_bf16 v[98:101], v[142:145], v[186:189], v[98:101]
	v_mfma_f32_16x16x32_bf16 v[86:89], v[134:137], v[196:199], v[86:89]
	v_mfma_f32_16x16x32_bf16 v[82:85], v[142:145], v[196:199], v[82:85]
	v_mfma_f32_16x16x32_bf16 v[70:73], v[134:137], v[216:219], v[70:73]
	v_mfma_f32_16x16x32_bf16 v[66:69], v[142:145], v[216:219], v[66:69]

.LBB0_289:
	s_ashr_i32 s27, s26, 31
	s_lshl_b64 s[26:27], s[26:27], 7
	s_add_u32 s58, s18, s26
	s_mov_b32 m0, s38
	s_addc_u32 s59, s19, s27
	ds_read_b128 v[174:177], v167 offset:16384
	ds_read_b128 v[178:181], v167 offset:17408
	ds_read_b128 v[182:185], v167 offset:18432
	ds_read_b128 v[186:189], v167 offset:19456
	ds_read_b128 v[190:193], v167 offset:20480
	ds_read_b128 v[196:199], v167 offset:21504
	ds_read_b128 v[200:203], v167 offset:22528
	ds_read_b128 v[216:219], v167 offset:23552
	global_load_lds_dwordx4 v164, s[58:59]
	s_mov_b32 m0, s39
	s_nop 0
	global_load_lds_dwordx4 v168, s[58:59]
	s_mov_b32 m0, s40
	s_nop 0
	global_load_lds_dwordx4 v166, s[58:59]
	s_mov_b32 m0, s41
	s_nop 0
	global_load_lds_dwordx4 v170, s[58:59]
	s_add_u32 s58, s10, s26
	s_addc_u32 s59, s11, s27
	v_lshl_add_u64 v[204:205], s[58:59], 0, v[194:195]
	s_mov_b32 m0, s13
	s_nop 0
	global_load_lds_dwordx4 v[204:205], off
	v_lshl_add_u64 v[204:205], s[58:59], 0, v[162:163]
	s_mov_b32 m0, s42
	s_nop 0
	global_load_lds_dwordx4 v[204:205], off
	s_cmp_lg_u32 s100, 0
	s_waitcnt vmcnt(8)
	s_waitcnt lgkmcnt(0)
	s_barrier
	s_setprio 1
	s_cbranch_scc1 .Lcz2_287
	v_mfma_f32_16x16x32_bf16 v[62:65], v[146:149], v[174:177], v[62:65]
	v_mfma_f32_16x16x32_bf16 v[58:61], v[154:157], v[174:177], v[58:61]
	v_mfma_f32_16x16x32_bf16 v[46:49], v[146:149], v[182:185], v[46:49]
	v_mfma_f32_16x16x32_bf16 v[42:45], v[154:157], v[182:185], v[42:45]
	v_mfma_f32_16x16x32_bf16 v[30:33], v[146:149], v[190:193], v[30:33]
	v_mfma_f32_16x16x32_bf16 v[26:29], v[154:157], v[190:193], v[26:29]
	v_mfma_f32_16x16x32_bf16 v[14:17], v[146:149], v[200:203], v[14:17]
	v_mfma_f32_16x16x32_bf16 v[10:13], v[154:157], v[200:203], v[10:13]
	v_mfma_f32_16x16x32_bf16 v[62:65], v[150:153], v[178:181], v[62:65]
	v_mfma_f32_16x16x32_bf16 v[58:61], v[158:161], v[178:181], v[58:61]
	v_mfma_f32_16x16x32_bf16 v[46:49], v[150:153], v[186:189], v[46:49]
	v_mfma_f32_16x16x32_bf16 v[42:45], v[158:161], v[186:189], v[42:45]
	v_mfma_f32_16x16x32_bf16 v[30:33], v[150:153], v[196:199], v[30:33]
	v_mfma_f32_16x16x32_bf16 v[26:29], v[158:161], v[196:199], v[26:29]
	v_mfma_f32_16x16x32_bf16 v[14:17], v[150:153], v[216:219], v[14:17]
	v_mfma_f32_16x16x32_bf16 v[10:13], v[158:161], v[216:219], v[10:13]
	s_setprio 0
	s_setprio 1
	v_mfma_f32_16x16x32_bf16 v[54:57], v[130:133], v[174:177], v[54:57]
	v_mfma_f32_16x16x32_bf16 v[50:53], v[138:141], v[174:177], v[50:53]
	v_mfma_f32_16x16x32_bf16 v[38:41], v[130:133], v[182:185], v[38:41]
	v_mfma_f32_16x16x32_bf16 v[34:37], v[138:141], v[182:185], v[34:37]
	v_mfma_f32_16x16x32_bf16 v[22:25], v[130:133], v[190:193], v[22:25]
	v_mfma_f32_16x16x32_bf16 v[18:21], v[138:141], v[190:193], v[18:21]
	v_mfma_f32_16x16x32_bf16 v[6:9], v[130:133], v[200:203], v[6:9]
	v_mfma_f32_16x16x32_bf16 v[2:5], v[138:141], v[200:203], v[2:5]
	v_mfma_f32_16x16x32_bf16 v[54:57], v[134:137], v[178:181], v[54:57]
	v_mfma_f32_16x16x32_bf16 v[50:53], v[142:145], v[178:181], v[50:53]
	v_mfma_f32_16x16x32_bf16 v[38:41], v[134:137], v[186:189], v[38:41]
	v_mfma_f32_16x16x32_bf16 v[34:37], v[142:145], v[186:189], v[34:37]
	v_mfma_f32_16x16x32_bf16 v[22:25], v[134:137], v[196:199], v[22:25]
	v_mfma_f32_16x16x32_bf16 v[18:21], v[142:145], v[196:199], v[18:21]
	v_mfma_f32_16x16x32_bf16 v[6:9], v[134:137], v[216:219], v[6:9]
	v_mfma_f32_16x16x32_bf16 v[2:5], v[142:145], v[216:219], v[2:5]
.Lcj2_287:
	s_setprio 0
	s_barrier
	v_add_u32_e32 v142, 0x18000, v165
	v_add_u32_e32 v158, 0x1c000, v165
	ds_read_b128 v[130:133], v142
	ds_read_b128 v[134:137], v142 offset:1024
	ds_read_b128 v[138:141], v142 offset:2048
	ds_read_b128 v[142:145], v142 offset:3072
	ds_read_b128 v[146:149], v158
	ds_read_b128 v[150:153], v158 offset:1024
	ds_read_b128 v[154:157], v158 offset:2048
	ds_read_b128 v[158:161], v158 offset:3072
	s_add_u32 s58, s58, 0x40000
	s_addc_u32 s59, s59, 0
	s_mov_b32 m0, s43
	v_lshl_add_u64 v[204:205], s[58:59], 0, v[194:195]
	ds_read_b128 v[174:177], v167 offset:32768
	ds_read_b128 v[178:181], v167 offset:33792
	ds_read_b128 v[182:185], v167 offset:34816
	ds_read_b128 v[186:189], v167 offset:35840
	ds_read_b128 v[190:193], v167 offset:36864
	ds_read_b128 v[196:199], v167 offset:37888
	ds_read_b128 v[200:203], v167 offset:38912
	ds_read_b128 v[216:219], v167 offset:39936
	global_load_lds_dwordx4 v[204:205], off
	v_lshl_add_u64 v[204:205], s[58:59], 0, v[162:163]
	s_mov_b32 m0, s44
	s_nop 0
	global_load_lds_dwordx4 v[204:205], off
	s_waitcnt vmcnt(8)
	s_waitcnt lgkmcnt(0)
	s_barrier
	s_setprio 1
	v_mfma_f32_16x16x32_bf16 v[126:129], v[130:133], v[174:177], v[126:129]
	v_mfma_f32_16x16x32_bf16 v[122:125], v[138:141], v[174:177], v[122:125]
	v_mfma_f32_16x16x32_bf16 v[110:113], v[130:133], v[182:185], v[110:113]
	v_mfma_f32_16x16x32_bf16 v[106:109], v[138:141], v[182:185], v[106:109]
	v_mfma_f32_16x16x32_bf16 v[94:97], v[130:133], v[190:193], v[94:97]
	v_mfma_f32_16x16x32_bf16 v[90:93], v[138:141], v[190:193], v[90:93]
	v_mfma_f32_16x16x32_bf16 v[78:81], v[130:133], v[200:203], v[78:81]
	v_mfma_f32_16x16x32_bf16 v[74:77], v[138:141], v[200:203], v[74:77]
	v_mfma_f32_16x16x32_bf16 v[126:129], v[134:137], v[178:181], v[126:129]
	v_mfma_f32_16x16x32_bf16 v[122:125], v[142:145], v[178:181], v[122:125]
	v_mfma_f32_16x16x32_bf16 v[110:113], v[134:137], v[186:189], v[110:113]
	v_mfma_f32_16x16x32_bf16 v[106:109], v[142:145], v[186:189], v[106:109]
	v_mfma_f32_16x16x32_bf16 v[94:97], v[134:137], v[196:199], v[94:97]
	v_mfma_f32_16x16x32_bf16 v[90:93], v[142:145], v[196:199], v[90:93]
	v_mfma_f32_16x16x32_bf16 v[78:81], v[134:137], v[216:219], v[78:81]
	v_mfma_f32_16x16x32_bf16 v[74:77], v[142:145], v[216:219], v[74:77]
	s_setprio 0
	s_setprio 1
	v_mfma_f32_16x16x32_bf16 v[118:121], v[146:149], v[174:177], v[118:121]
	v_mfma_f32_16x16x32_bf16 v[114:117], v[154:157], v[174:177], v[114:117]
	v_mfma_f32_16x16x32_bf16 v[102:105], v[146:149], v[182:185], v[102:105]
	v_mfma_f32_16x16x32_bf16 v[98:101], v[154:157], v[182:185], v[98:101]
	v_mfma_f32_16x16x32_bf16 v[86:89], v[146:149], v[190:193], v[86:89]
	v_mfma_f32_16x16x32_bf16 v[82:85], v[154:157], v[190:193], v[82:85]
	v_mfma_f32_16x16x32_bf16 v[70:73], v[146:149], v[200:203], v[70:73]
	v_mfma_f32_16x16x32_bf16 v[66:69], v[154:157], v[200:203], v[66:69]
	v_mfma_f32_16x16x32_bf16 v[118:121], v[150:153], v[178:181], v[118:121]
	v_mfma_f32_16x16x32_bf16 v[114:117], v[158:161], v[178:181], v[114:117]
	v_mfma_f32_16x16x32_bf16 v[102:105], v[150:153], v[186:189], v[102:105]
	v_mfma_f32_16x16x32_bf16 v[98:101], v[158:161], v[186:189], v[98:101]
	v_mfma_f32_16x16x32_bf16 v[86:89], v[150:153], v[196:199], v[86:89]
	v_mfma_f32_16x16x32_bf16 v[82:85], v[158:161], v[196:199], v[82:85]
	v_mfma_f32_16x16x32_bf16 v[70:73], v[150:153], v[216:219], v[70:73]
	v_mfma_f32_16x16x32_bf16 v[66:69], v[158:161], v[216:219], v[66:69]
	s_setprio 0
	s_barrier
	s_add_u32 s57, s26, 0x80
	s_addc_u32 s58, s27, 0
	s_add_u32 s26, s18, s57
	s_mov_b32 m0, s46
	s_addc_u32 s27, s19, s58
	ds_read_b128 v[174:177], v167 offset:49152
	ds_read_b128 v[178:181], v167 offset:50176
	ds_read_b128 v[182:185], v167 offset:51200
	ds_read_b128 v[186:189], v167 offset:52224
	ds_read_b128 v[190:193], v167 offset:53248
	ds_read_b128 v[196:199], v167 offset:54272
	ds_read_b128 v[200:203], v167 offset:55296
	ds_read_b128 v[216:219], v167 offset:56320
	global_load_lds_dwordx4 v164, s[26:27]
	s_mov_b32 m0, s47
	s_nop 0
	global_load_lds_dwordx4 v168, s[26:27]
	s_mov_b32 m0, s50
	s_nop 0
	global_load_lds_dwordx4 v166, s[26:27]
	s_mov_b32 m0, s51
	s_nop 0
	global_load_lds_dwordx4 v170, s[26:27]
	s_add_u32 s26, s10, s57
	s_addc_u32 s27, s11, s58
	v_lshl_add_u64 v[204:205], s[26:27], 0, v[194:195]
	s_mov_b32 m0, s48
	s_nop 0
	global_load_lds_dwordx4 v[204:205], off
	v_lshl_add_u64 v[204:205], s[26:27], 0, v[162:163]
	s_mov_b32 m0, s49
	s_nop 0
	global_load_lds_dwordx4 v[204:205], off
	s_waitcnt vmcnt(8)
	s_waitcnt lgkmcnt(0)
	s_barrier
	s_setprio 1
	v_mfma_f32_16x16x32_bf16 v[62:65], v[130:133], v[174:177], v[62:65]
	v_mfma_f32_16x16x32_bf16 v[58:61], v[138:141], v[174:177], v[58:61]
	v_mfma_f32_16x16x32_bf16 v[46:49], v[130:133], v[182:185], v[46:49]
	v_mfma_f32_16x16x32_bf16 v[42:45], v[138:141], v[182:185], v[42:45]
	v_mfma_f32_16x16x32_bf16 v[30:33], v[130:133], v[190:193], v[30:33]
	v_mfma_f32_16x16x32_bf16 v[26:29], v[138:141], v[190:193], v[26:29]
	v_mfma_f32_16x16x32_bf16 v[14:17], v[130:133], v[200:203], v[14:17]
	v_mfma_f32_16x16x32_bf16 v[10:13], v[138:141], v[200:203], v[10:13]
	v_mfma_f32_16x16x32_bf16 v[62:65], v[134:137], v[178:181], v[62:65]
	v_mfma_f32_16x16x32_bf16 v[58:61], v[142:145], v[178:181], v[58:61]
	v_mfma_f32_16x16x32_bf16 v[46:49], v[134:137], v[186:189], v[46:49]
	v_mfma_f32_16x16x32_bf16 v[42:45], v[142:145], v[186:189], v[42:45]
	v_mfma_f32_16x16x32_bf16 v[30:33], v[134:137], v[196:199], v[30:33]
	v_mfma_f32_16x16x32_bf16 v[26:29], v[142:145], v[196:199], v[26:29]
	v_mfma_f32_16x16x32_bf16 v[14:17], v[134:137], v[216:219], v[14:17]
	v_mfma_f32_16x16x32_bf16 v[10:13], v[142:145], v[216:219], v[10:13]
	s_setprio 0
	s_setprio 1
	v_mfma_f32_16x16x32_bf16 v[54:57], v[146:149], v[174:177], v[54:57]
	v_mfma_f32_16x16x32_bf16 v[50:53], v[154:157], v[174:177], v[50:53]
	v_mfma_f32_16x16x32_bf16 v[38:41], v[146:149], v[182:185], v[38:41]
	v_mfma_f32_16x16x32_bf16 v[34:37], v[154:157], v[182:185], v[34:37]
	v_mfma_f32_16x16x32_bf16 v[22:25], v[146:149], v[190:193], v[22:25]
	v_mfma_f32_16x16x32_bf16 v[18:21], v[154:157], v[190:193], v[18:21]
	v_mfma_f32_16x16x32_bf16 v[6:9], v[146:149], v[200:203], v[6:9]
	v_mfma_f32_16x16x32_bf16 v[2:5], v[154:157], v[200:203], v[2:5]
	v_mfma_f32_16x16x32_bf16 v[54:57], v[150:153], v[178:181], v[54:57]
	v_mfma_f32_16x16x32_bf16 v[50:53], v[158:161], v[178:181], v[50:53]
	v_mfma_f32_16x16x32_bf16 v[38:41], v[150:153], v[186:189], v[38:41]
	v_mfma_f32_16x16x32_bf16 v[34:37], v[158:161], v[186:189], v[34:37]
	v_mfma_f32_16x16x32_bf16 v[22:25], v[150:153], v[196:199], v[22:25]
	v_mfma_f32_16x16x32_bf16 v[18:21], v[158:161], v[196:199], v[18:21]
	v_mfma_f32_16x16x32_bf16 v[6:9], v[150:153], v[216:219], v[6:9]
	v_mfma_f32_16x16x32_bf16 v[2:5], v[158:161], v[216:219], v[2:5]
	s_setprio 0
	s_barrier
	s_add_i32 s26, s56, 2
	s_add_u32 s24, s24, 0x100
	s_addc_u32 s25, s25, 0
	s_cmp_ge_i32 s56, s55
	s_cbranch_scc1 .LBB0_292
	s_mov_b32 s56, s26
	s_branch .LBB0_287

.LBB0_374:
	v_add_u32_e32 v142, 0x10000, v217
	v_add_u32_e32 v158, 0x14000, v217
	ds_read_b128 v[130:133], v142
	ds_read_b128 v[134:137], v142 offset:1024
	ds_read_b128 v[138:141], v142 offset:2048
	ds_read_b128 v[142:145], v142 offset:3072
	ds_read_b128 v[146:149], v158
	ds_read_b128 v[150:153], v158 offset:1024
	ds_read_b128 v[154:157], v158 offset:2048
	ds_read_b128 v[158:161], v158 offset:3072
	s_add_i32 m0, s37, 0xc000
	s_add_i32 s57, s37, 0xe000
	s_cmp_eq_u32 s54, s56
	s_cselect_b64 s[58:59], -1, 0
	v_lshl_add_u64 v[196:197], s[20:21], 0, v[194:195]
	v_lshl_add_u64 v[196:197], v[196:197], 0, s[24:25]
	v_mov_b32_e32 v219, v195
	ds_read_b128 v[162:165], v221
	ds_read_b128 v[166:169], v221 offset:1024
	ds_read_b128 v[170:173], v221 offset:2048
	ds_read_b128 v[174:177], v221 offset:3072
	ds_read_b128 v[178:181], v221 offset:4096
	ds_read_b128 v[182:185], v221 offset:5120
	ds_read_b128 v[186:189], v221 offset:6144
	ds_read_b128 v[190:193], v221 offset:7168
	global_load_lds_dwordx4 v[196:197], off
	v_lshl_add_u64 v[196:197], s[20:21], 0, v[218:219]
	v_lshl_add_u64 v[196:197], v[196:197], 0, s[24:25]
	s_mov_b32 m0, s57
	s_nop 0
	global_load_lds_dwordx4 v[196:197], off
	s_cmp_lg_u32 s100, 0
	s_waitcnt vmcnt(8)
	s_waitcnt lgkmcnt(0)
	s_barrier
	s_setprio 1
	s_cbranch_scc1 .Lcz1_374
	v_mfma_f32_16x16x32_bf16 v[126:129], v[130:133], v[162:165], v[126:129]
	v_mfma_f32_16x16x32_bf16 v[122:125], v[138:141], v[162:165], v[122:125]
	v_mfma_f32_16x16x32_bf16 v[94:97], v[130:133], v[170:173], v[94:97]
	v_mfma_f32_16x16x32_bf16 v[86:89], v[138:141], v[170:173], v[86:89]
	v_mfma_f32_16x16x32_bf16 v[62:65], v[130:133], v[178:181], v[62:65]
	v_mfma_f32_16x16x32_bf16 v[54:57], v[138:141], v[178:181], v[54:57]
	v_mfma_f32_16x16x32_bf16 v[30:33], v[130:133], v[186:189], v[30:33]
	v_mfma_f32_16x16x32_bf16 v[22:25], v[138:141], v[186:189], v[22:25]
	v_mfma_f32_16x16x32_bf16 v[126:129], v[134:137], v[166:169], v[126:129]
	v_mfma_f32_16x16x32_bf16 v[122:125], v[142:145], v[166:169], v[122:125]
	v_mfma_f32_16x16x32_bf16 v[94:97], v[134:137], v[174:177], v[94:97]
	v_mfma_f32_16x16x32_bf16 v[86:89], v[142:145], v[174:177], v[86:89]
	v_mfma_f32_16x16x32_bf16 v[62:65], v[134:137], v[182:185], v[62:65]
	v_mfma_f32_16x16x32_bf16 v[54:57], v[142:145], v[182:185], v[54:57]
	v_mfma_f32_16x16x32_bf16 v[30:33], v[134:137], v[190:193], v[30:33]
	v_mfma_f32_16x16x32_bf16 v[22:25], v[142:145], v[190:193], v[22:25]
	s_setprio 0
	s_setprio 1
	v_mfma_f32_16x16x32_bf16 v[110:113], v[146:149], v[162:165], v[110:113]
	v_mfma_f32_16x16x32_bf16 v[102:105], v[154:157], v[162:165], v[102:105]
	v_mfma_f32_16x16x32_bf16 v[78:81], v[146:149], v[170:173], v[78:81]
	v_mfma_f32_16x16x32_bf16 v[70:73], v[154:157], v[170:173], v[70:73]
	v_mfma_f32_16x16x32_bf16 v[46:49], v[146:149], v[178:181], v[46:49]
	v_mfma_f32_16x16x32_bf16 v[38:41], v[154:157], v[178:181], v[38:41]
	v_mfma_f32_16x16x32_bf16 v[14:17], v[146:149], v[186:189], v[14:17]
	v_mfma_f32_16x16x32_bf16 v[6:9], v[154:157], v[186:189], v[6:9]
	v_mfma_f32_16x16x32_bf16 v[110:113], v[150:153], v[166:169], v[110:113]
	v_mfma_f32_16x16x32_bf16 v[102:105], v[158:161], v[166:169], v[102:105]
	v_mfma_f32_16x16x32_bf16 v[78:81], v[150:153], v[174:177], v[78:81]
	v_mfma_f32_16x16x32_bf16 v[70:73], v[158:161], v[174:177], v[70:73]
	v_mfma_f32_16x16x32_bf16 v[46:49], v[150:153], v[182:185], v[46:49]
	v_mfma_f32_16x16x32_bf16 v[38:41], v[158:161], v[182:185], v[38:41]
	v_mfma_f32_16x16x32_bf16 v[14:17], v[150:153], v[190:193], v[14:17]
	v_mfma_f32_16x16x32_bf16 v[6:9], v[158:161], v[190:193], v[6:9]
.Lcj1_374:
	s_setprio 0
	s_barrier
	s_and_b64 s[60:61], s[58:59], exec
	s_cselect_b32 s62, 0, s56
	s_and_b64 s[58:59], s[2:3], s[58:59]
	s_and_b64 s[58:59], s[58:59], exec
	s_cselect_b32 s9, s55, s9
	s_cselect_b32 s8, s23, s8
	s_cselect_b32 s21, s7, s21
	s_cselect_b32 s20, s6, s20
	s_lshl_b64 s[58:59], s[62:63], 7
	s_add_u32 s60, s8, s58
	s_addc_u32 s61, s9, s59
	s_mov_b32 m0, s38
	s_add_u32 s57, s8, 0x8000
	ds_read_b128 v[162:165], v221 offset:16384
	ds_read_b128 v[166:169], v221 offset:17408
	ds_read_b128 v[170:173], v221 offset:18432
	ds_read_b128 v[174:177], v221 offset:19456
	ds_read_b128 v[178:181], v221 offset:20480
	ds_read_b128 v[182:185], v221 offset:21504
	ds_read_b128 v[186:189], v221 offset:22528
	ds_read_b128 v[190:193], v221 offset:23552
	global_load_lds_dwordx4 v216, s[60:61]
	s_mov_b32 m0, s39
	s_addc_u32 s66, s9, 0
	global_load_lds_dwordx4 v220, s[60:61]
	s_add_u32 s60, s57, s58
	s_addc_u32 s61, s66, s59
	s_mov_b32 m0, s40
	s_add_u32 s58, s20, s58
	global_load_lds_dwordx4 v216, s[60:61]
	s_mov_b32 m0, s41
	s_addc_u32 s59, s21, s59
	global_load_lds_dwordx4 v220, s[60:61]
	s_mov_b32 m0, s37
	s_nop 0
	global_load_lds_dwordx4 v194, s[58:59]
	s_mov_b32 m0, s42
	s_nop 0
	global_load_lds_dwordx4 v218, s[58:59]
	s_cmp_lg_u32 s100, 0
	s_waitcnt vmcnt(8)
	s_waitcnt lgkmcnt(0)
	s_barrier
	s_setprio 1
	s_cbranch_scc1 .Lcz2_374
	v_mfma_f32_16x16x32_bf16 v[118:121], v[130:133], v[162:165], v[118:121]
	v_mfma_f32_16x16x32_bf16 v[114:117], v[138:141], v[162:165], v[114:117]
	v_mfma_f32_16x16x32_bf16 v[90:93], v[130:133], v[170:173], v[90:93]
	v_mfma_f32_16x16x32_bf16 v[82:85], v[138:141], v[170:173], v[82:85]
	v_mfma_f32_16x16x32_bf16 v[58:61], v[130:133], v[178:181], v[58:61]
	v_mfma_f32_16x16x32_bf16 v[50:53], v[138:141], v[178:181], v[50:53]
	v_mfma_f32_16x16x32_bf16 v[26:29], v[130:133], v[186:189], v[26:29]
	v_mfma_f32_16x16x32_bf16 v[18:21], v[138:141], v[186:189], v[18:21]
	v_mfma_f32_16x16x32_bf16 v[118:121], v[134:137], v[166:169], v[118:121]
	v_mfma_f32_16x16x32_bf16 v[114:117], v[142:145], v[166:169], v[114:117]
	v_mfma_f32_16x16x32_bf16 v[90:93], v[134:137], v[174:177], v[90:93]
	v_mfma_f32_16x16x32_bf16 v[82:85], v[142:145], v[174:177], v[82:85]
	v_mfma_f32_16x16x32_bf16 v[58:61], v[134:137], v[182:185], v[58:61]
	v_mfma_f32_16x16x32_bf16 v[50:53], v[142:145], v[182:185], v[50:53]
	v_mfma_f32_16x16x32_bf16 v[26:29], v[134:137], v[190:193], v[26:29]
	v_mfma_f32_16x16x32_bf16 v[18:21], v[142:145], v[190:193], v[18:21]
	s_setprio 0
	s_setprio 1
	v_mfma_f32_16x16x32_bf16 v[106:109], v[146:149], v[162:165], v[106:109]
	v_mfma_f32_16x16x32_bf16 v[98:101], v[154:157], v[162:165], v[98:101]
	v_mfma_f32_16x16x32_bf16 v[74:77], v[146:149], v[170:173], v[74:77]
	v_mfma_f32_16x16x32_bf16 v[66:69], v[154:157], v[170:173], v[66:69]
	v_mfma_f32_16x16x32_bf16 v[42:45], v[146:149], v[178:181], v[42:45]
	v_mfma_f32_16x16x32_bf16 v[34:37], v[154:157], v[178:181], v[34:37]
	v_mfma_f32_16x16x32_bf16 v[10:13], v[146:149], v[186:189], v[10:13]
	v_mfma_f32_16x16x32_bf16 v[2:5], v[154:157], v[186:189], v[2:5]
	v_mfma_f32_16x16x32_bf16 v[106:109], v[150:153], v[166:169], v[106:109]
	v_mfma_f32_16x16x32_bf16 v[98:101], v[158:161], v[166:169], v[98:101]
	v_mfma_f32_16x16x32_bf16 v[74:77], v[150:153], v[174:177], v[74:77]
	v_mfma_f32_16x16x32_bf16 v[66:69], v[158:161], v[174:177], v[66:69]
	v_mfma_f32_16x16x32_bf16 v[42:45], v[150:153], v[182:185], v[42:45]
	v_mfma_f32_16x16x32_bf16 v[34:37], v[158:161], v[182:185], v[34:37]
	v_mfma_f32_16x16x32_bf16 v[10:13], v[150:153], v[190:193], v[10:13]
	v_mfma_f32_16x16x32_bf16 v[2:5], v[158:161], v[190:193], v[2:5]
.Lcj2_374:
	s_setprio 0
	s_barrier
	v_add_u32_e32 v142, 0x18000, v217
	v_add_u32_e32 v158, 0x1c000, v217
	ds_read_b128 v[130:133], v142
	ds_read_b128 v[134:137], v142 offset:1024
	ds_read_b128 v[138:141], v142 offset:2048
	ds_read_b128 v[142:145], v142 offset:3072
	ds_read_b128 v[146:149], v158
	ds_read_b128 v[150:153], v158 offset:1024
	ds_read_b128 v[154:157], v158 offset:2048
	ds_read_b128 v[158:161], v158 offset:3072
	s_add_u32 s58, s58, 0x8000
	s_addc_u32 s59, s59, 0
	s_mov_b32 m0, s43
	ds_read_b128 v[162:165], v221 offset:32768
	ds_read_b128 v[166:169], v221 offset:33792
	ds_read_b128 v[170:173], v221 offset:34816
	ds_read_b128 v[174:177], v221 offset:35840
	ds_read_b128 v[178:181], v221 offset:36864
	ds_read_b128 v[182:185], v221 offset:37888
	ds_read_b128 v[186:189], v221 offset:38912
	ds_read_b128 v[190:193], v221 offset:39936
	global_load_lds_dwordx4 v194, s[58:59]
	s_mov_b32 m0, s44
	s_nop 0
	global_load_lds_dwordx4 v218, s[58:59]
	s_waitcnt vmcnt(8)
	s_waitcnt lgkmcnt(0)
	s_barrier
	s_setprio 1
	v_mfma_f32_16x16x32_bf16 v[126:129], v[130:133], v[162:165], v[126:129]
	v_mfma_f32_16x16x32_bf16 v[122:125], v[138:141], v[162:165], v[122:125]
	v_mfma_f32_16x16x32_bf16 v[94:97], v[130:133], v[170:173], v[94:97]
	v_mfma_f32_16x16x32_bf16 v[86:89], v[138:141], v[170:173], v[86:89]
	v_mfma_f32_16x16x32_bf16 v[62:65], v[130:133], v[178:181], v[62:65]
	v_mfma_f32_16x16x32_bf16 v[54:57], v[138:141], v[178:181], v[54:57]
	v_mfma_f32_16x16x32_bf16 v[30:33], v[130:133], v[186:189], v[30:33]
	v_mfma_f32_16x16x32_bf16 v[22:25], v[138:141], v[186:189], v[22:25]
	v_mfma_f32_16x16x32_bf16 v[126:129], v[134:137], v[166:169], v[126:129]
	v_mfma_f32_16x16x32_bf16 v[122:125], v[142:145], v[166:169], v[122:125]
	v_mfma_f32_16x16x32_bf16 v[94:97], v[134:137], v[174:177], v[94:97]
	v_mfma_f32_16x16x32_bf16 v[86:89], v[142:145], v[174:177], v[86:89]
	v_mfma_f32_16x16x32_bf16 v[62:65], v[134:137], v[182:185], v[62:65]
	v_mfma_f32_16x16x32_bf16 v[54:57], v[142:145], v[182:185], v[54:57]
	v_mfma_f32_16x16x32_bf16 v[30:33], v[134:137], v[190:193], v[30:33]
	v_mfma_f32_16x16x32_bf16 v[22:25], v[142:145], v[190:193], v[22:25]
	s_setprio 0
	s_setprio 1
	v_mfma_f32_16x16x32_bf16 v[110:113], v[146:149], v[162:165], v[110:113]
	v_mfma_f32_16x16x32_bf16 v[102:105], v[154:157], v[162:165], v[102:105]
	v_mfma_f32_16x16x32_bf16 v[78:81], v[146:149], v[170:173], v[78:81]
	v_mfma_f32_16x16x32_bf16 v[70:73], v[154:157], v[170:173], v[70:73]
	v_mfma_f32_16x16x32_bf16 v[46:49], v[146:149], v[178:181], v[46:49]
	v_mfma_f32_16x16x32_bf16 v[38:41], v[154:157], v[178:181], v[38:41]
	v_mfma_f32_16x16x32_bf16 v[14:17], v[146:149], v[186:189], v[14:17]
	v_mfma_f32_16x16x32_bf16 v[6:9], v[154:157], v[186:189], v[6:9]
	v_mfma_f32_16x16x32_bf16 v[110:113], v[150:153], v[166:169], v[110:113]
	v_mfma_f32_16x16x32_bf16 v[102:105], v[158:161], v[166:169], v[102:105]
	v_mfma_f32_16x16x32_bf16 v[78:81], v[150:153], v[174:177], v[78:81]
	v_mfma_f32_16x16x32_bf16 v[70:73], v[158:161], v[174:177], v[70:73]
	v_mfma_f32_16x16x32_bf16 v[46:49], v[150:153], v[182:185], v[46:49]
	v_mfma_f32_16x16x32_bf16 v[38:41], v[158:161], v[182:185], v[38:41]
	v_mfma_f32_16x16x32_bf16 v[14:17], v[150:153], v[190:193], v[14:17]
	v_mfma_f32_16x16x32_bf16 v[6:9], v[158:161], v[190:193], v[6:9]
	s_setprio 0
	s_barrier
	s_or_b32 s62, s62, 1
	s_lshl_b64 s[58:59], s[62:63], 7
	s_add_u32 s60, s8, s58
	s_mov_b32 m0, s45
	s_addc_u32 s61, s9, s59
	ds_read_b128 v[162:165], v221 offset:49152
	ds_read_b128 v[166:169], v221 offset:50176
	ds_read_b128 v[170:173], v221 offset:51200
	ds_read_b128 v[174:177], v221 offset:52224
	ds_read_b128 v[178:181], v221 offset:53248
	ds_read_b128 v[182:185], v221 offset:54272
	ds_read_b128 v[186:189], v221 offset:55296
	ds_read_b128 v[190:193], v221 offset:56320
	global_load_lds_dwordx4 v216, s[60:61]
	s_mov_b32 m0, s46
	s_nop 0
	global_load_lds_dwordx4 v220, s[60:61]
	s_add_u32 s60, s57, s58
	s_addc_u32 s61, s66, s59
	s_mov_b32 m0, s49
	s_add_u32 s58, s20, s58
	global_load_lds_dwordx4 v216, s[60:61]
	s_mov_b32 m0, s50
	s_addc_u32 s59, s21, s59
	global_load_lds_dwordx4 v220, s[60:61]
	s_mov_b32 m0, s47
	s_nop 0
	global_load_lds_dwordx4 v194, s[58:59]
	s_mov_b32 m0, s48
	s_nop 0
	global_load_lds_dwordx4 v218, s[58:59]
	s_waitcnt vmcnt(8)
	s_waitcnt lgkmcnt(0)
	s_barrier
	s_setprio 1
	v_mfma_f32_16x16x32_bf16 v[118:121], v[130:133], v[162:165], v[118:121]
	v_mfma_f32_16x16x32_bf16 v[114:117], v[138:141], v[162:165], v[114:117]
	v_mfma_f32_16x16x32_bf16 v[90:93], v[130:133], v[170:173], v[90:93]
	v_mfma_f32_16x16x32_bf16 v[82:85], v[138:141], v[170:173], v[82:85]
	v_mfma_f32_16x16x32_bf16 v[58:61], v[130:133], v[178:181], v[58:61]
	v_mfma_f32_16x16x32_bf16 v[50:53], v[138:141], v[178:181], v[50:53]
	v_mfma_f32_16x16x32_bf16 v[26:29], v[130:133], v[186:189], v[26:29]
	v_mfma_f32_16x16x32_bf16 v[18:21], v[138:141], v[186:189], v[18:21]
	v_mfma_f32_16x16x32_bf16 v[118:121], v[134:137], v[166:169], v[118:121]
	v_mfma_f32_16x16x32_bf16 v[114:117], v[142:145], v[166:169], v[114:117]
	v_mfma_f32_16x16x32_bf16 v[90:93], v[134:137], v[174:177], v[90:93]
	v_mfma_f32_16x16x32_bf16 v[82:85], v[142:145], v[174:177], v[82:85]
	v_mfma_f32_16x16x32_bf16 v[58:61], v[134:137], v[182:185], v[58:61]
	v_mfma_f32_16x16x32_bf16 v[50:53], v[142:145], v[182:185], v[50:53]
	v_mfma_f32_16x16x32_bf16 v[26:29], v[134:137], v[190:193], v[26:29]
	v_mfma_f32_16x16x32_bf16 v[18:21], v[142:145], v[190:193], v[18:21]
	s_setprio 0
	s_setprio 1
	v_mfma_f32_16x16x32_bf16 v[106:109], v[146:149], v[162:165], v[106:109]
	v_mfma_f32_16x16x32_bf16 v[98:101], v[154:157], v[162:165], v[98:101]
	v_mfma_f32_16x16x32_bf16 v[74:77], v[146:149], v[170:173], v[74:77]
	v_mfma_f32_16x16x32_bf16 v[66:69], v[154:157], v[170:173], v[66:69]
	v_mfma_f32_16x16x32_bf16 v[42:45], v[146:149], v[178:181], v[42:45]
	v_mfma_f32_16x16x32_bf16 v[34:37], v[154:157], v[178:181], v[34:37]
	v_mfma_f32_16x16x32_bf16 v[10:13], v[146:149], v[186:189], v[10:13]
	v_mfma_f32_16x16x32_bf16 v[2:5], v[154:157], v[186:189], v[2:5]
	v_mfma_f32_16x16x32_bf16 v[106:109], v[150:153], v[166:169], v[106:109]
	v_mfma_f32_16x16x32_bf16 v[98:101], v[158:161], v[166:169], v[98:101]
	v_mfma_f32_16x16x32_bf16 v[74:77], v[150:153], v[174:177], v[74:77]
	v_mfma_f32_16x16x32_bf16 v[66:69], v[158:161], v[174:177], v[66:69]
	v_mfma_f32_16x16x32_bf16 v[42:45], v[150:153], v[182:185], v[42:45]
	v_mfma_f32_16x16x32_bf16 v[34:37], v[158:161], v[182:185], v[34:37]
	v_mfma_f32_16x16x32_bf16 v[10:13], v[150:153], v[190:193], v[10:13]
	v_mfma_f32_16x16x32_bf16 v[2:5], v[158:161], v[190:193], v[2:5]
	s_setprio 0
	s_barrier
	s_add_i32 s57, s56, 2
	s_add_u32 s24, s24, 0x100
	s_addc_u32 s25, s25, 0
	s_cmp_ge_i32 s56, s54
	s_mov_b32 s56, s57
	s_cbranch_scc0 .LBB0_374
	s_branch .Lcsk_374

.LBB0_492:
	v_add_u32_e32 v130, 0x10000, v165
	v_add_u32_e32 v142, 0x14000, v165
	ds_read_b128 v[146:149], v130
	ds_read_b128 v[150:153], v130 offset:1024
	ds_read_b128 v[154:157], v130 offset:2048
	ds_read_b128 v[158:161], v130 offset:3072
	ds_read_b128 v[130:133], v142
	ds_read_b128 v[134:137], v142 offset:1024
	ds_read_b128 v[138:141], v142 offset:2048
	ds_read_b128 v[142:145], v142 offset:3072
	s_add_i32 m0, s29, 0xc000
	s_add_i32 s24, s29, 0xe000
	s_cmp_lg_u32 s52, s55
	s_cselect_b64 s[56:57], -1, 0
	v_lshl_add_u64 v[204:205], s[16:17], 0, v[194:195]
	v_lshl_add_u64 v[204:205], v[204:205], 0, s[22:23]
	v_mov_b32_e32 v163, v195
	ds_read_b128 v[174:177], v167
	ds_read_b128 v[178:181], v167 offset:1024
	ds_read_b128 v[182:185], v167 offset:2048
	ds_read_b128 v[186:189], v167 offset:3072
	ds_read_b128 v[190:193], v167 offset:4096
	ds_read_b128 v[196:199], v167 offset:5120
	ds_read_b128 v[200:203], v167 offset:6144
	ds_read_b128 v[216:219], v167 offset:7168
	global_load_lds_dwordx4 v[204:205], off
	v_lshl_add_u64 v[204:205], s[16:17], 0, v[162:163]
	v_lshl_add_u64 v[204:205], v[204:205], 0, s[22:23]
	s_mov_b32 m0, s24
	s_nop 0
	global_load_lds_dwordx4 v[204:205], off
	s_cmp_lg_u32 s100, 0
	s_waitcnt vmcnt(8)
	s_waitcnt lgkmcnt(0)
	s_barrier
	s_setprio 1
	s_cbranch_scc1 .Lcz1_492
	v_mfma_f32_16x16x32_bf16 v[126:129], v[146:149], v[174:177], v[126:129]
	v_mfma_f32_16x16x32_bf16 v[122:125], v[154:157], v[174:177], v[122:125]
	v_mfma_f32_16x16x32_bf16 v[110:113], v[146:149], v[182:185], v[110:113]
	v_mfma_f32_16x16x32_bf16 v[106:109], v[154:157], v[182:185], v[106:109]
	v_mfma_f32_16x16x32_bf16 v[94:97], v[146:149], v[190:193], v[94:97]
	v_mfma_f32_16x16x32_bf16 v[90:93], v[154:157], v[190:193], v[90:93]
	v_mfma_f32_16x16x32_bf16 v[78:81], v[146:149], v[200:203], v[78:81]
	v_mfma_f32_16x16x32_bf16 v[74:77], v[154:157], v[200:203], v[74:77]
	v_mfma_f32_16x16x32_bf16 v[126:129], v[150:153], v[178:181], v[126:129]
	v_mfma_f32_16x16x32_bf16 v[122:125], v[158:161], v[178:181], v[122:125]
	v_mfma_f32_16x16x32_bf16 v[110:113], v[150:153], v[186:189], v[110:113]
	v_mfma_f32_16x16x32_bf16 v[106:109], v[158:161], v[186:189], v[106:109]
	v_mfma_f32_16x16x32_bf16 v[94:97], v[150:153], v[196:199], v[94:97]
	v_mfma_f32_16x16x32_bf16 v[90:93], v[158:161], v[196:199], v[90:93]
	v_mfma_f32_16x16x32_bf16 v[78:81], v[150:153], v[216:219], v[78:81]
	v_mfma_f32_16x16x32_bf16 v[74:77], v[158:161], v[216:219], v[74:77]
	s_setprio 0
	s_setprio 1
	v_mfma_f32_16x16x32_bf16 v[118:121], v[130:133], v[174:177], v[118:121]
	v_mfma_f32_16x16x32_bf16 v[114:117], v[138:141], v[174:177], v[114:117]
	v_mfma_f32_16x16x32_bf16 v[102:105], v[130:133], v[182:185], v[102:105]
	v_mfma_f32_16x16x32_bf16 v[98:101], v[138:141], v[182:185], v[98:101]
	v_mfma_f32_16x16x32_bf16 v[86:89], v[130:133], v[190:193], v[86:89]
	v_mfma_f32_16x16x32_bf16 v[82:85], v[138:141], v[190:193], v[82:85]
	v_mfma_f32_16x16x32_bf16 v[70:73], v[130:133], v[200:203], v[70:73]
	v_mfma_f32_16x16x32_bf16 v[66:69], v[138:141], v[200:203], v[66:69]
	v_mfma_f32_16x16x32_bf16 v[118:121], v[134:137], v[178:181], v[118:121]
	v_mfma_f32_16x16x32_bf16 v[114:117], v[142:145], v[178:181], v[114:117]
	v_mfma_f32_16x16x32_bf16 v[102:105], v[134:137], v[186:189], v[102:105]
	v_mfma_f32_16x16x32_bf16 v[98:101], v[142:145], v[186:189], v[98:101]
	v_mfma_f32_16x16x32_bf16 v[86:89], v[134:137], v[196:199], v[86:89]
	v_mfma_f32_16x16x32_bf16 v[82:85], v[142:145], v[196:199], v[82:85]
	v_mfma_f32_16x16x32_bf16 v[70:73], v[134:137], v[216:219], v[70:73]
	v_mfma_f32_16x16x32_bf16 v[66:69], v[142:145], v[216:219], v[66:69]

.LBB0_494:
	s_ashr_i32 s25, s24, 31
	s_lshl_b64 s[24:25], s[24:25], 7
	s_add_u32 s56, s14, s24
	s_mov_b32 m0, s30
	s_addc_u32 s57, s15, s25
	ds_read_b128 v[174:177], v167 offset:16384
	ds_read_b128 v[178:181], v167 offset:17408
	ds_read_b128 v[182:185], v167 offset:18432
	ds_read_b128 v[186:189], v167 offset:19456
	ds_read_b128 v[190:193], v167 offset:20480
	ds_read_b128 v[196:199], v167 offset:21504
	ds_read_b128 v[200:203], v167 offset:22528
	ds_read_b128 v[216:219], v167 offset:23552
	global_load_lds_dwordx4 v164, s[56:57]
	s_mov_b32 m0, s31
	s_nop 0
	global_load_lds_dwordx4 v168, s[56:57]
	s_mov_b32 m0, s37
	s_nop 0
	global_load_lds_dwordx4 v166, s[56:57]
	s_mov_b32 m0, s38
	s_nop 0
	global_load_lds_dwordx4 v170, s[56:57]
	s_add_u32 s56, s16, s24
	s_addc_u32 s57, s17, s25
	v_lshl_add_u64 v[204:205], s[56:57], 0, v[194:195]
	s_mov_b32 m0, s29
	s_nop 0
	global_load_lds_dwordx4 v[204:205], off
	v_lshl_add_u64 v[204:205], s[56:57], 0, v[162:163]
	s_mov_b32 m0, s39
	s_nop 0
	global_load_lds_dwordx4 v[204:205], off
	s_cmp_lg_u32 s100, 0
	s_waitcnt vmcnt(8)
	s_waitcnt lgkmcnt(0)
	s_barrier
	s_setprio 1
	s_cbranch_scc1 .Lcz2_492
	v_mfma_f32_16x16x32_bf16 v[62:65], v[146:149], v[174:177], v[62:65]
	v_mfma_f32_16x16x32_bf16 v[58:61], v[154:157], v[174:177], v[58:61]
	v_mfma_f32_16x16x32_bf16 v[46:49], v[146:149], v[182:185], v[46:49]
	v_mfma_f32_16x16x32_bf16 v[42:45], v[154:157], v[182:185], v[42:45]
	v_mfma_f32_16x16x32_bf16 v[30:33], v[146:149], v[190:193], v[30:33]
	v_mfma_f32_16x16x32_bf16 v[26:29], v[154:157], v[190:193], v[26:29]
	v_mfma_f32_16x16x32_bf16 v[14:17], v[146:149], v[200:203], v[14:17]
	v_mfma_f32_16x16x32_bf16 v[10:13], v[154:157], v[200:203], v[10:13]
	v_mfma_f32_16x16x32_bf16 v[62:65], v[150:153], v[178:181], v[62:65]
	v_mfma_f32_16x16x32_bf16 v[58:61], v[158:161], v[178:181], v[58:61]
	v_mfma_f32_16x16x32_bf16 v[46:49], v[150:153], v[186:189], v[46:49]
	v_mfma_f32_16x16x32_bf16 v[42:45], v[158:161], v[186:189], v[42:45]
	v_mfma_f32_16x16x32_bf16 v[30:33], v[150:153], v[196:199], v[30:33]
	v_mfma_f32_16x16x32_bf16 v[26:29], v[158:161], v[196:199], v[26:29]
	v_mfma_f32_16x16x32_bf16 v[14:17], v[150:153], v[216:219], v[14:17]
	v_mfma_f32_16x16x32_bf16 v[10:13], v[158:161], v[216:219], v[10:13]
	s_setprio 0
	s_setprio 1
	v_mfma_f32_16x16x32_bf16 v[54:57], v[130:133], v[174:177], v[54:57]
	v_mfma_f32_16x16x32_bf16 v[50:53], v[138:141], v[174:177], v[50:53]
	v_mfma_f32_16x16x32_bf16 v[38:41], v[130:133], v[182:185], v[38:41]
	v_mfma_f32_16x16x32_bf16 v[34:37], v[138:141], v[182:185], v[34:37]
	v_mfma_f32_16x16x32_bf16 v[22:25], v[130:133], v[190:193], v[22:25]
	v_mfma_f32_16x16x32_bf16 v[18:21], v[138:141], v[190:193], v[18:21]
	v_mfma_f32_16x16x32_bf16 v[6:9], v[130:133], v[200:203], v[6:9]
	v_mfma_f32_16x16x32_bf16 v[2:5], v[138:141], v[200:203], v[2:5]
	v_mfma_f32_16x16x32_bf16 v[54:57], v[134:137], v[178:181], v[54:57]
	v_mfma_f32_16x16x32_bf16 v[50:53], v[142:145], v[178:181], v[50:53]
	v_mfma_f32_16x16x32_bf16 v[38:41], v[134:137], v[186:189], v[38:41]
	v_mfma_f32_16x16x32_bf16 v[34:37], v[142:145], v[186:189], v[34:37]
	v_mfma_f32_16x16x32_bf16 v[22:25], v[134:137], v[196:199], v[22:25]
	v_mfma_f32_16x16x32_bf16 v[18:21], v[142:145], v[196:199], v[18:21]
	v_mfma_f32_16x16x32_bf16 v[6:9], v[134:137], v[216:219], v[6:9]
	v_mfma_f32_16x16x32_bf16 v[2:5], v[142:145], v[216:219], v[2:5]
.Lcj2_492:
	s_setprio 0
	s_barrier
	v_add_u32_e32 v142, 0x18000, v165
	v_add_u32_e32 v158, 0x1c000, v165
	ds_read_b128 v[130:133], v142
	ds_read_b128 v[134:137], v142 offset:1024
	ds_read_b128 v[138:141], v142 offset:2048
	ds_read_b128 v[142:145], v142 offset:3072
	ds_read_b128 v[146:149], v158
	ds_read_b128 v[150:153], v158 offset:1024
	ds_read_b128 v[154:157], v158 offset:2048
	ds_read_b128 v[158:161], v158 offset:3072
	s_add_u32 s56, s56, 0x10000
	s_addc_u32 s57, s57, 0
	s_mov_b32 m0, s40
	v_lshl_add_u64 v[204:205], s[56:57], 0, v[194:195]
	ds_read_b128 v[174:177], v167 offset:32768
	ds_read_b128 v[178:181], v167 offset:33792
	ds_read_b128 v[182:185], v167 offset:34816
	ds_read_b128 v[186:189], v167 offset:35840
	ds_read_b128 v[190:193], v167 offset:36864
	ds_read_b128 v[196:199], v167 offset:37888
	ds_read_b128 v[200:203], v167 offset:38912
	ds_read_b128 v[216:219], v167 offset:39936
	global_load_lds_dwordx4 v[204:205], off
	v_lshl_add_u64 v[204:205], s[56:57], 0, v[162:163]
	s_mov_b32 m0, s41
	s_nop 0
	global_load_lds_dwordx4 v[204:205], off
	s_waitcnt vmcnt(8)
	s_waitcnt lgkmcnt(0)
	s_barrier
	s_setprio 1
	v_mfma_f32_16x16x32_bf16 v[126:129], v[130:133], v[174:177], v[126:129]
	v_mfma_f32_16x16x32_bf16 v[122:125], v[138:141], v[174:177], v[122:125]
	v_mfma_f32_16x16x32_bf16 v[110:113], v[130:133], v[182:185], v[110:113]
	v_mfma_f32_16x16x32_bf16 v[106:109], v[138:141], v[182:185], v[106:109]
	v_mfma_f32_16x16x32_bf16 v[94:97], v[130:133], v[190:193], v[94:97]
	v_mfma_f32_16x16x32_bf16 v[90:93], v[138:141], v[190:193], v[90:93]
	v_mfma_f32_16x16x32_bf16 v[78:81], v[130:133], v[200:203], v[78:81]
	v_mfma_f32_16x16x32_bf16 v[74:77], v[138:141], v[200:203], v[74:77]
	v_mfma_f32_16x16x32_bf16 v[126:129], v[134:137], v[178:181], v[126:129]
	v_mfma_f32_16x16x32_bf16 v[122:125], v[142:145], v[178:181], v[122:125]
	v_mfma_f32_16x16x32_bf16 v[110:113], v[134:137], v[186:189], v[110:113]
	v_mfma_f32_16x16x32_bf16 v[106:109], v[142:145], v[186:189], v[106:109]
	v_mfma_f32_16x16x32_bf16 v[94:97], v[134:137], v[196:199], v[94:97]
	v_mfma_f32_16x16x32_bf16 v[90:93], v[142:145], v[196:199], v[90:93]
	v_mfma_f32_16x16x32_bf16 v[78:81], v[134:137], v[216:219], v[78:81]
	v_mfma_f32_16x16x32_bf16 v[74:77], v[142:145], v[216:219], v[74:77]
	s_setprio 0
	s_setprio 1
	v_mfma_f32_16x16x32_bf16 v[118:121], v[146:149], v[174:177], v[118:121]
	v_mfma_f32_16x16x32_bf16 v[114:117], v[154:157], v[174:177], v[114:117]
	v_mfma_f32_16x16x32_bf16 v[102:105], v[146:149], v[182:185], v[102:105]
	v_mfma_f32_16x16x32_bf16 v[98:101], v[154:157], v[182:185], v[98:101]
	v_mfma_f32_16x16x32_bf16 v[86:89], v[146:149], v[190:193], v[86:89]
	v_mfma_f32_16x16x32_bf16 v[82:85], v[154:157], v[190:193], v[82:85]
	v_mfma_f32_16x16x32_bf16 v[70:73], v[146:149], v[200:203], v[70:73]
	v_mfma_f32_16x16x32_bf16 v[66:69], v[154:157], v[200:203], v[66:69]
	v_mfma_f32_16x16x32_bf16 v[118:121], v[150:153], v[178:181], v[118:121]
	v_mfma_f32_16x16x32_bf16 v[114:117], v[158:161], v[178:181], v[114:117]
	v_mfma_f32_16x16x32_bf16 v[102:105], v[150:153], v[186:189], v[102:105]
	v_mfma_f32_16x16x32_bf16 v[98:101], v[158:161], v[186:189], v[98:101]
	v_mfma_f32_16x16x32_bf16 v[86:89], v[150:153], v[196:199], v[86:89]
	v_mfma_f32_16x16x32_bf16 v[82:85], v[158:161], v[196:199], v[82:85]
	v_mfma_f32_16x16x32_bf16 v[70:73], v[150:153], v[216:219], v[70:73]
	v_mfma_f32_16x16x32_bf16 v[66:69], v[158:161], v[216:219], v[66:69]
	s_setprio 0
	s_barrier
	s_add_u32 s56, s24, 0x80
	s_addc_u32 s57, s25, 0
	s_add_u32 s24, s14, s56
	s_mov_b32 m0, s43
	s_addc_u32 s25, s15, s57
	ds_read_b128 v[174:177], v167 offset:49152
	ds_read_b128 v[178:181], v167 offset:50176
	ds_read_b128 v[182:185], v167 offset:51200
	ds_read_b128 v[186:189], v167 offset:52224
	ds_read_b128 v[190:193], v167 offset:53248
	ds_read_b128 v[196:199], v167 offset:54272
	ds_read_b128 v[200:203], v167 offset:55296
	ds_read_b128 v[216:219], v167 offset:56320
	global_load_lds_dwordx4 v164, s[24:25]
	s_mov_b32 m0, s44
	s_nop 0
	global_load_lds_dwordx4 v168, s[24:25]
	s_mov_b32 m0, s47
	s_nop 0
	global_load_lds_dwordx4 v166, s[24:25]
	s_mov_b32 m0, s48
	s_nop 0
	global_load_lds_dwordx4 v170, s[24:25]
	s_add_u32 s24, s16, s56
	s_addc_u32 s25, s17, s57
	v_lshl_add_u64 v[204:205], s[24:25], 0, v[194:195]
	s_mov_b32 m0, s45
	s_nop 0
	global_load_lds_dwordx4 v[204:205], off
	v_lshl_add_u64 v[204:205], s[24:25], 0, v[162:163]
	s_mov_b32 m0, s46
	s_nop 0
	global_load_lds_dwordx4 v[204:205], off
	s_waitcnt vmcnt(8)
	s_waitcnt lgkmcnt(0)
	s_barrier
	s_setprio 1
	v_mfma_f32_16x16x32_bf16 v[62:65], v[130:133], v[174:177], v[62:65]
	v_mfma_f32_16x16x32_bf16 v[58:61], v[138:141], v[174:177], v[58:61]
	v_mfma_f32_16x16x32_bf16 v[46:49], v[130:133], v[182:185], v[46:49]
	v_mfma_f32_16x16x32_bf16 v[42:45], v[138:141], v[182:185], v[42:45]
	v_mfma_f32_16x16x32_bf16 v[30:33], v[130:133], v[190:193], v[30:33]
	v_mfma_f32_16x16x32_bf16 v[26:29], v[138:141], v[190:193], v[26:29]
	v_mfma_f32_16x16x32_bf16 v[14:17], v[130:133], v[200:203], v[14:17]
	v_mfma_f32_16x16x32_bf16 v[10:13], v[138:141], v[200:203], v[10:13]
	v_mfma_f32_16x16x32_bf16 v[62:65], v[134:137], v[178:181], v[62:65]
	v_mfma_f32_16x16x32_bf16 v[58:61], v[142:145], v[178:181], v[58:61]
	v_mfma_f32_16x16x32_bf16 v[46:49], v[134:137], v[186:189], v[46:49]
	v_mfma_f32_16x16x32_bf16 v[42:45], v[142:145], v[186:189], v[42:45]
	v_mfma_f32_16x16x32_bf16 v[30:33], v[134:137], v[196:199], v[30:33]
	v_mfma_f32_16x16x32_bf16 v[26:29], v[142:145], v[196:199], v[26:29]
	v_mfma_f32_16x16x32_bf16 v[14:17], v[134:137], v[216:219], v[14:17]
	v_mfma_f32_16x16x32_bf16 v[10:13], v[142:145], v[216:219], v[10:13]
	s_setprio 0
	s_setprio 1
	v_mfma_f32_16x16x32_bf16 v[54:57], v[146:149], v[174:177], v[54:57]
	v_mfma_f32_16x16x32_bf16 v[50:53], v[154:157], v[174:177], v[50:53]
	v_mfma_f32_16x16x32_bf16 v[38:41], v[146:149], v[182:185], v[38:41]
	v_mfma_f32_16x16x32_bf16 v[34:37], v[154:157], v[182:185], v[34:37]
	v_mfma_f32_16x16x32_bf16 v[22:25], v[146:149], v[190:193], v[22:25]
	v_mfma_f32_16x16x32_bf16 v[18:21], v[154:157], v[190:193], v[18:21]
	v_mfma_f32_16x16x32_bf16 v[6:9], v[146:149], v[200:203], v[6:9]
	v_mfma_f32_16x16x32_bf16 v[2:5], v[154:157], v[200:203], v[2:5]
	v_mfma_f32_16x16x32_bf16 v[54:57], v[150:153], v[178:181], v[54:57]
	v_mfma_f32_16x16x32_bf16 v[50:53], v[158:161], v[178:181], v[50:53]
	v_mfma_f32_16x16x32_bf16 v[38:41], v[150:153], v[186:189], v[38:41]
	v_mfma_f32_16x16x32_bf16 v[34:37], v[158:161], v[186:189], v[34:37]
	v_mfma_f32_16x16x32_bf16 v[22:25], v[150:153], v[196:199], v[22:25]
	v_mfma_f32_16x16x32_bf16 v[18:21], v[158:161], v[196:199], v[18:21]
	v_mfma_f32_16x16x32_bf16 v[6:9], v[150:153], v[216:219], v[6:9]
	v_mfma_f32_16x16x32_bf16 v[2:5], v[158:161], v[216:219], v[2:5]
	s_setprio 0
	s_barrier
	s_add_i32 s24, s55, 2
	s_add_u32 s22, s22, 0x100
	s_addc_u32 s23, s23, 0
	s_cmp_ge_i32 s55, s52
	s_cbranch_scc1 .LBB0_497
	s_mov_b32 s55, s24
	s_branch .LBB0_492

.LBB0_581:
	v_add_u32_e32 v142, 0x10000, v191
	v_add_u32_e32 v158, 0x14000, v191
	ds_read_b128 v[130:133], v142
	ds_read_b128 v[134:137], v142 offset:1024
	ds_read_b128 v[138:141], v142 offset:2048
	ds_read_b128 v[142:145], v142 offset:3072
	ds_read_b128 v[146:149], v158
	ds_read_b128 v[150:153], v158 offset:1024
	ds_read_b128 v[154:157], v158 offset:2048
	ds_read_b128 v[158:161], v158 offset:3072
	s_add_i32 m0, s31, 0xc000
	s_add_i32 s62, s31, 0xe000
	s_add_i32 s66, s61, 2
	s_cmp_eq_u32 s59, s61
	s_cselect_b64 s[68:69], -1, 0
	v_lshl_add_u64 v[200:201], s[0:1], 0, v[194:195]
	v_lshl_add_u64 v[200:201], v[200:201], 0, s[22:23]
	v_mov_b32_e32 v193, v195
	ds_read_b128 v[162:165], v217
	ds_read_b128 v[166:169], v217 offset:1024
	ds_read_b128 v[170:173], v217 offset:2048
	ds_read_b128 v[174:177], v217 offset:3072
	ds_read_b128 v[178:181], v217 offset:4096
	ds_read_b128 v[182:185], v217 offset:5120
	ds_read_b128 v[186:189], v217 offset:6144
	ds_read_b128 v[196:199], v217 offset:7168
	global_load_lds_dwordx4 v[200:201], off
	v_lshl_add_u64 v[200:201], s[0:1], 0, v[192:193]
	v_lshl_add_u64 v[200:201], v[200:201], 0, s[22:23]
	s_mov_b32 m0, s62
	s_nop 0
	global_load_lds_dwordx4 v[200:201], off
	s_cmp_lg_u32 s100, 0
	s_waitcnt vmcnt(8)
	s_waitcnt lgkmcnt(0)
	s_barrier
	s_setprio 1
	s_cbranch_scc1 .Lcz1_579
	v_mfma_f32_16x16x32_bf16 v[122:125], v[130:133], v[162:165], v[122:125]
	v_mfma_f32_16x16x32_bf16 v[126:129], v[138:141], v[162:165], v[126:129]
	v_mfma_f32_16x16x32_bf16 v[110:113], v[130:133], v[170:173], v[110:113]
	v_mfma_f32_16x16x32_bf16 v[106:109], v[138:141], v[170:173], v[106:109]
	v_mfma_f32_16x16x32_bf16 v[94:97], v[130:133], v[178:181], v[94:97]
	v_mfma_f32_16x16x32_bf16 v[90:93], v[138:141], v[178:181], v[90:93]
	v_mfma_f32_16x16x32_bf16 v[78:81], v[130:133], v[186:189], v[78:81]
	v_mfma_f32_16x16x32_bf16 v[74:77], v[138:141], v[186:189], v[74:77]
	v_mfma_f32_16x16x32_bf16 v[122:125], v[134:137], v[166:169], v[122:125]
	v_mfma_f32_16x16x32_bf16 v[126:129], v[142:145], v[166:169], v[126:129]
	v_mfma_f32_16x16x32_bf16 v[110:113], v[134:137], v[174:177], v[110:113]
	v_mfma_f32_16x16x32_bf16 v[106:109], v[142:145], v[174:177], v[106:109]
	v_mfma_f32_16x16x32_bf16 v[94:97], v[134:137], v[182:185], v[94:97]
	v_mfma_f32_16x16x32_bf16 v[90:93], v[142:145], v[182:185], v[90:93]
	v_mfma_f32_16x16x32_bf16 v[78:81], v[134:137], v[196:199], v[78:81]
	v_mfma_f32_16x16x32_bf16 v[74:77], v[142:145], v[196:199], v[74:77]
	s_setprio 0
	s_setprio 1
	v_mfma_f32_16x16x32_bf16 v[118:121], v[146:149], v[162:165], v[118:121]
	v_mfma_f32_16x16x32_bf16 v[114:117], v[154:157], v[162:165], v[114:117]
	v_mfma_f32_16x16x32_bf16 v[102:105], v[146:149], v[170:173], v[102:105]
	v_mfma_f32_16x16x32_bf16 v[98:101], v[154:157], v[170:173], v[98:101]
	v_mfma_f32_16x16x32_bf16 v[86:89], v[146:149], v[178:181], v[86:89]
	v_mfma_f32_16x16x32_bf16 v[82:85], v[154:157], v[178:181], v[82:85]
	v_mfma_f32_16x16x32_bf16 v[70:73], v[146:149], v[186:189], v[70:73]
	v_mfma_f32_16x16x32_bf16 v[66:69], v[154:157], v[186:189], v[66:69]
	v_mfma_f32_16x16x32_bf16 v[118:121], v[150:153], v[166:169], v[118:121]
	v_mfma_f32_16x16x32_bf16 v[114:117], v[158:161], v[166:169], v[114:117]
	v_mfma_f32_16x16x32_bf16 v[102:105], v[150:153], v[174:177], v[102:105]
	v_mfma_f32_16x16x32_bf16 v[98:101], v[158:161], v[174:177], v[98:101]
	v_mfma_f32_16x16x32_bf16 v[86:89], v[150:153], v[182:185], v[86:89]
	v_mfma_f32_16x16x32_bf16 v[82:85], v[158:161], v[182:185], v[82:85]
	v_mfma_f32_16x16x32_bf16 v[70:73], v[150:153], v[196:199], v[70:73]
	v_mfma_f32_16x16x32_bf16 v[66:69], v[158:161], v[196:199], v[66:69]
.Lcj1_579:
	s_setprio 0
	s_barrier
	s_and_b64 s[72:73], s[68:69], exec
	s_cselect_b32 s62, 0, s66
	s_and_b64 s[68:69], s[4:5], s[68:69]
	s_and_b64 s[68:69], s[68:69], exec
	s_cselect_b32 s7, s19, s7
	s_cselect_b32 s6, s18, s6
	s_cselect_b32 s1, s17, s1
	s_cselect_b32 s0, s16, s0
	s_lshl_b64 s[68:69], s[62:63], 7
	s_add_u32 s72, s6, s68
	s_addc_u32 s73, s7, s69
	s_mov_b32 m0, s37
	s_add_u32 s61, s6, 0x60000
	ds_read_b128 v[162:165], v217 offset:16384
	ds_read_b128 v[166:169], v217 offset:17408
	ds_read_b128 v[170:173], v217 offset:18432
	ds_read_b128 v[174:177], v217 offset:19456
	ds_read_b128 v[178:181], v217 offset:20480
	ds_read_b128 v[182:185], v217 offset:21504
	ds_read_b128 v[186:189], v217 offset:22528
	ds_read_b128 v[196:199], v217 offset:23552
	global_load_lds_dwordx4 v190, s[72:73]
	s_mov_b32 m0, s38
	s_addc_u32 s67, s7, 0
	global_load_lds_dwordx4 v216, s[72:73]
	s_add_u32 s72, s61, s68
	s_addc_u32 s73, s67, s69
	s_mov_b32 m0, s39
	s_add_u32 s68, s0, s68
	global_load_lds_dwordx4 v190, s[72:73]
	s_mov_b32 m0, s40
	s_addc_u32 s69, s1, s69
	global_load_lds_dwordx4 v216, s[72:73]
	s_mov_b32 m0, s31
	s_nop 0
	global_load_lds_dwordx4 v194, s[68:69]
	s_mov_b32 m0, s41
	s_nop 0
	global_load_lds_dwordx4 v192, s[68:69]
	s_cmp_lg_u32 s100, 0
	s_waitcnt vmcnt(8)
	s_waitcnt lgkmcnt(0)
	s_barrier
	s_setprio 1
	s_cbranch_scc1 .Lcz2_579
	v_mfma_f32_16x16x32_bf16 v[62:65], v[130:133], v[162:165], v[62:65]
	v_mfma_f32_16x16x32_bf16 v[58:61], v[138:141], v[162:165], v[58:61]
	v_mfma_f32_16x16x32_bf16 v[46:49], v[130:133], v[170:173], v[46:49]
	v_mfma_f32_16x16x32_bf16 v[42:45], v[138:141], v[170:173], v[42:45]
	v_mfma_f32_16x16x32_bf16 v[30:33], v[130:133], v[178:181], v[30:33]
	v_mfma_f32_16x16x32_bf16 v[26:29], v[138:141], v[178:181], v[26:29]
	v_mfma_f32_16x16x32_bf16 v[14:17], v[130:133], v[186:189], v[14:17]
	v_mfma_f32_16x16x32_bf16 v[10:13], v[138:141], v[186:189], v[10:13]
	v_mfma_f32_16x16x32_bf16 v[62:65], v[134:137], v[166:169], v[62:65]
	v_mfma_f32_16x16x32_bf16 v[58:61], v[142:145], v[166:169], v[58:61]
	v_mfma_f32_16x16x32_bf16 v[46:49], v[134:137], v[174:177], v[46:49]
	v_mfma_f32_16x16x32_bf16 v[42:45], v[142:145], v[174:177], v[42:45]
	v_mfma_f32_16x16x32_bf16 v[30:33], v[134:137], v[182:185], v[30:33]
	v_mfma_f32_16x16x32_bf16 v[26:29], v[142:145], v[182:185], v[26:29]
	v_mfma_f32_16x16x32_bf16 v[14:17], v[134:137], v[196:199], v[14:17]
	v_mfma_f32_16x16x32_bf16 v[10:13], v[142:145], v[196:199], v[10:13]
	s_setprio 0
	s_setprio 1
	v_mfma_f32_16x16x32_bf16 v[54:57], v[146:149], v[162:165], v[54:57]
	v_mfma_f32_16x16x32_bf16 v[50:53], v[154:157], v[162:165], v[50:53]
	v_mfma_f32_16x16x32_bf16 v[38:41], v[146:149], v[170:173], v[38:41]
	v_mfma_f32_16x16x32_bf16 v[34:37], v[154:157], v[170:173], v[34:37]
	v_mfma_f32_16x16x32_bf16 v[22:25], v[146:149], v[178:181], v[22:25]
	v_mfma_f32_16x16x32_bf16 v[18:21], v[154:157], v[178:181], v[18:21]
	v_mfma_f32_16x16x32_bf16 v[6:9], v[146:149], v[186:189], v[6:9]
	v_mfma_f32_16x16x32_bf16 v[2:5], v[154:157], v[186:189], v[2:5]
	v_mfma_f32_16x16x32_bf16 v[54:57], v[150:153], v[166:169], v[54:57]
	v_mfma_f32_16x16x32_bf16 v[50:53], v[158:161], v[166:169], v[50:53]
	v_mfma_f32_16x16x32_bf16 v[38:41], v[150:153], v[174:177], v[38:41]
	v_mfma_f32_16x16x32_bf16 v[34:37], v[158:161], v[174:177], v[34:37]
	v_mfma_f32_16x16x32_bf16 v[22:25], v[150:153], v[182:185], v[22:25]
	v_mfma_f32_16x16x32_bf16 v[18:21], v[158:161], v[182:185], v[18:21]
	v_mfma_f32_16x16x32_bf16 v[6:9], v[150:153], v[196:199], v[6:9]
	v_mfma_f32_16x16x32_bf16 v[2:5], v[158:161], v[196:199], v[2:5]
.Lcj2_579:
	s_setprio 0
	s_barrier
	v_add_u32_e32 v142, 0x18000, v191
	v_add_u32_e32 v158, 0x1c000, v191
	ds_read_b128 v[130:133], v142
	ds_read_b128 v[134:137], v142 offset:1024
	ds_read_b128 v[138:141], v142 offset:2048
	ds_read_b128 v[142:145], v142 offset:3072
	ds_read_b128 v[146:149], v158
	ds_read_b128 v[150:153], v158 offset:1024
	ds_read_b128 v[154:157], v158 offset:2048
	ds_read_b128 v[158:161], v158 offset:3072
	s_add_u32 s68, s68, 0x60000
	s_addc_u32 s69, s69, 0
	s_mov_b32 m0, s42
	ds_read_b128 v[162:165], v217 offset:32768
	ds_read_b128 v[166:169], v217 offset:33792
	ds_read_b128 v[170:173], v217 offset:34816
	ds_read_b128 v[174:177], v217 offset:35840
	ds_read_b128 v[178:181], v217 offset:36864
	ds_read_b128 v[182:185], v217 offset:37888
	ds_read_b128 v[186:189], v217 offset:38912
	ds_read_b128 v[196:199], v217 offset:39936
	global_load_lds_dwordx4 v194, s[68:69]
	s_mov_b32 m0, s43
	s_nop 0
	global_load_lds_dwordx4 v192, s[68:69]
	s_waitcnt vmcnt(8)
	s_waitcnt lgkmcnt(0)
	s_barrier
	s_setprio 1
	v_mfma_f32_16x16x32_bf16 v[122:125], v[130:133], v[162:165], v[122:125]
	v_mfma_f32_16x16x32_bf16 v[126:129], v[138:141], v[162:165], v[126:129]
	v_mfma_f32_16x16x32_bf16 v[110:113], v[130:133], v[170:173], v[110:113]
	v_mfma_f32_16x16x32_bf16 v[106:109], v[138:141], v[170:173], v[106:109]
	v_mfma_f32_16x16x32_bf16 v[94:97], v[130:133], v[178:181], v[94:97]
	v_mfma_f32_16x16x32_bf16 v[90:93], v[138:141], v[178:181], v[90:93]
	v_mfma_f32_16x16x32_bf16 v[78:81], v[130:133], v[186:189], v[78:81]
	v_mfma_f32_16x16x32_bf16 v[74:77], v[138:141], v[186:189], v[74:77]
	v_mfma_f32_16x16x32_bf16 v[122:125], v[134:137], v[166:169], v[122:125]
	v_mfma_f32_16x16x32_bf16 v[126:129], v[142:145], v[166:169], v[126:129]
	v_mfma_f32_16x16x32_bf16 v[110:113], v[134:137], v[174:177], v[110:113]
	v_mfma_f32_16x16x32_bf16 v[106:109], v[142:145], v[174:177], v[106:109]
	v_mfma_f32_16x16x32_bf16 v[94:97], v[134:137], v[182:185], v[94:97]
	v_mfma_f32_16x16x32_bf16 v[90:93], v[142:145], v[182:185], v[90:93]
	v_mfma_f32_16x16x32_bf16 v[78:81], v[134:137], v[196:199], v[78:81]
	v_mfma_f32_16x16x32_bf16 v[74:77], v[142:145], v[196:199], v[74:77]
	s_setprio 0
	s_setprio 1
	v_mfma_f32_16x16x32_bf16 v[118:121], v[146:149], v[162:165], v[118:121]
	v_mfma_f32_16x16x32_bf16 v[114:117], v[154:157], v[162:165], v[114:117]
	v_mfma_f32_16x16x32_bf16 v[102:105], v[146:149], v[170:173], v[102:105]
	v_mfma_f32_16x16x32_bf16 v[98:101], v[154:157], v[170:173], v[98:101]
	v_mfma_f32_16x16x32_bf16 v[86:89], v[146:149], v[178:181], v[86:89]
	v_mfma_f32_16x16x32_bf16 v[82:85], v[154:157], v[178:181], v[82:85]
	v_mfma_f32_16x16x32_bf16 v[70:73], v[146:149], v[186:189], v[70:73]
	v_mfma_f32_16x16x32_bf16 v[66:69], v[154:157], v[186:189], v[66:69]
	v_mfma_f32_16x16x32_bf16 v[118:121], v[150:153], v[166:169], v[118:121]
	v_mfma_f32_16x16x32_bf16 v[114:117], v[158:161], v[166:169], v[114:117]
	v_mfma_f32_16x16x32_bf16 v[102:105], v[150:153], v[174:177], v[102:105]
	v_mfma_f32_16x16x32_bf16 v[98:101], v[158:161], v[174:177], v[98:101]
	v_mfma_f32_16x16x32_bf16 v[86:89], v[150:153], v[182:185], v[86:89]
	v_mfma_f32_16x16x32_bf16 v[82:85], v[158:161], v[182:185], v[82:85]
	v_mfma_f32_16x16x32_bf16 v[70:73], v[150:153], v[196:199], v[70:73]
	v_mfma_f32_16x16x32_bf16 v[66:69], v[158:161], v[196:199], v[66:69]
	s_setprio 0
	s_barrier
	s_or_b32 s62, s62, 1
	s_lshl_b64 s[68:69], s[62:63], 7
	s_add_u32 s72, s6, s68
	s_mov_b32 m0, s46
	s_addc_u32 s73, s7, s69
	ds_read_b128 v[162:165], v217 offset:49152
	ds_read_b128 v[166:169], v217 offset:50176
	ds_read_b128 v[170:173], v217 offset:51200
	ds_read_b128 v[174:177], v217 offset:52224
	ds_read_b128 v[178:181], v217 offset:53248
	ds_read_b128 v[182:185], v217 offset:54272
	ds_read_b128 v[186:189], v217 offset:55296
	ds_read_b128 v[196:199], v217 offset:56320
	global_load_lds_dwordx4 v190, s[72:73]
	s_mov_b32 m0, s47
	s_nop 0
	global_load_lds_dwordx4 v216, s[72:73]
	s_add_u32 s72, s61, s68
	s_addc_u32 s73, s67, s69
	s_mov_b32 m0, s50
	s_add_u32 s68, s0, s68
	global_load_lds_dwordx4 v190, s[72:73]
	s_mov_b32 m0, s51
	s_addc_u32 s69, s1, s69
	global_load_lds_dwordx4 v216, s[72:73]
	s_mov_b32 m0, s48
	s_nop 0
	global_load_lds_dwordx4 v194, s[68:69]
	s_mov_b32 m0, s49
	s_nop 0
	global_load_lds_dwordx4 v192, s[68:69]
	s_waitcnt vmcnt(8)
	s_waitcnt lgkmcnt(0)
	s_barrier
	s_setprio 1
	v_mfma_f32_16x16x32_bf16 v[62:65], v[130:133], v[162:165], v[62:65]
	v_mfma_f32_16x16x32_bf16 v[58:61], v[138:141], v[162:165], v[58:61]
	v_mfma_f32_16x16x32_bf16 v[46:49], v[130:133], v[170:173], v[46:49]
	v_mfma_f32_16x16x32_bf16 v[42:45], v[138:141], v[170:173], v[42:45]
	v_mfma_f32_16x16x32_bf16 v[30:33], v[130:133], v[178:181], v[30:33]
	v_mfma_f32_16x16x32_bf16 v[26:29], v[138:141], v[178:181], v[26:29]
	v_mfma_f32_16x16x32_bf16 v[14:17], v[130:133], v[186:189], v[14:17]
	v_mfma_f32_16x16x32_bf16 v[10:13], v[138:141], v[186:189], v[10:13]
	v_mfma_f32_16x16x32_bf16 v[62:65], v[134:137], v[166:169], v[62:65]
	v_mfma_f32_16x16x32_bf16 v[58:61], v[142:145], v[166:169], v[58:61]
	v_mfma_f32_16x16x32_bf16 v[46:49], v[134:137], v[174:177], v[46:49]
	v_mfma_f32_16x16x32_bf16 v[42:45], v[142:145], v[174:177], v[42:45]
	v_mfma_f32_16x16x32_bf16 v[30:33], v[134:137], v[182:185], v[30:33]
	v_mfma_f32_16x16x32_bf16 v[26:29], v[142:145], v[182:185], v[26:29]
	v_mfma_f32_16x16x32_bf16 v[14:17], v[134:137], v[196:199], v[14:17]
	v_mfma_f32_16x16x32_bf16 v[10:13], v[142:145], v[196:199], v[10:13]
	s_setprio 0
	s_setprio 1
	v_mfma_f32_16x16x32_bf16 v[54:57], v[146:149], v[162:165], v[54:57]
	v_mfma_f32_16x16x32_bf16 v[50:53], v[154:157], v[162:165], v[50:53]
	v_mfma_f32_16x16x32_bf16 v[38:41], v[146:149], v[170:173], v[38:41]
	v_mfma_f32_16x16x32_bf16 v[34:37], v[154:157], v[170:173], v[34:37]
	v_mfma_f32_16x16x32_bf16 v[22:25], v[146:149], v[178:181], v[22:25]
	v_mfma_f32_16x16x32_bf16 v[18:21], v[154:157], v[178:181], v[18:21]
	v_mfma_f32_16x16x32_bf16 v[6:9], v[146:149], v[186:189], v[6:9]
	v_mfma_f32_16x16x32_bf16 v[2:5], v[154:157], v[186:189], v[2:5]
	v_mfma_f32_16x16x32_bf16 v[54:57], v[150:153], v[166:169], v[54:57]
	v_mfma_f32_16x16x32_bf16 v[50:53], v[158:161], v[166:169], v[50:53]
	v_mfma_f32_16x16x32_bf16 v[38:41], v[150:153], v[174:177], v[38:41]
	v_mfma_f32_16x16x32_bf16 v[34:37], v[158:161], v[174:177], v[34:37]
	v_mfma_f32_16x16x32_bf16 v[22:25], v[150:153], v[182:185], v[22:25]
	v_mfma_f32_16x16x32_bf16 v[18:21], v[158:161], v[182:185], v[18:21]
	v_mfma_f32_16x16x32_bf16 v[6:9], v[150:153], v[196:199], v[6:9]
	v_mfma_f32_16x16x32_bf16 v[2:5], v[158:161], v[196:199], v[2:5]
	s_setprio 0
	s_barrier
	s_add_u32 s22, s22, 0x100
	s_addc_u32 s23, s23, 0
	s_cmp_ge_i32 s66, s58
	s_cbranch_scc1 .LBB0_583
	s_mov_b32 s61, s66
	s_mov_b32 s73, 0x10000
	s_branch .LBB0_579

.LBB0_662:
	v_add_u32_e32 v142, 0x10000, v191
	v_add_u32_e32 v158, 0x14000, v191
	ds_read_b128 v[130:133], v142
	ds_read_b128 v[134:137], v142 offset:1024
	ds_read_b128 v[138:141], v142 offset:2048
	ds_read_b128 v[142:145], v142 offset:3072
	ds_read_b128 v[146:149], v158
	ds_read_b128 v[150:153], v158 offset:1024
	ds_read_b128 v[154:157], v158 offset:2048
	ds_read_b128 v[158:161], v158 offset:3072
	s_add_i32 m0, s31, 0xc000
	s_add_i32 s58, s31, 0xe000
	s_cmp_eq_u32 s52, s55
	s_cselect_b64 s[56:57], -1, 0
	v_lshl_add_u64 v[200:201], s[0:1], 0, v[194:195]
	v_lshl_add_u64 v[200:201], v[200:201], 0, s[22:23]
	v_mov_b32_e32 v193, v195
	ds_read_b128 v[162:165], v217
	ds_read_b128 v[166:169], v217 offset:1024
	ds_read_b128 v[170:173], v217 offset:2048
	ds_read_b128 v[174:177], v217 offset:3072
	ds_read_b128 v[178:181], v217 offset:4096
	ds_read_b128 v[182:185], v217 offset:5120
	ds_read_b128 v[186:189], v217 offset:6144
	ds_read_b128 v[196:199], v217 offset:7168
	global_load_lds_dwordx4 v[200:201], off
	v_lshl_add_u64 v[200:201], s[0:1], 0, v[192:193]
	v_lshl_add_u64 v[200:201], v[200:201], 0, s[22:23]
	s_mov_b32 m0, s58
	s_nop 0
	global_load_lds_dwordx4 v[200:201], off
	s_cmp_lg_u32 s100, 0
	s_waitcnt vmcnt(8)
	s_waitcnt lgkmcnt(0)
	s_barrier
	s_setprio 1
	s_cbranch_scc1 .Lcz1_662
	v_mfma_f32_16x16x32_bf16 v[126:129], v[130:133], v[162:165], v[126:129]
	v_mfma_f32_16x16x32_bf16 v[122:125], v[138:141], v[162:165], v[122:125]
	v_mfma_f32_16x16x32_bf16 v[110:113], v[130:133], v[170:173], v[110:113]
	v_mfma_f32_16x16x32_bf16 v[106:109], v[138:141], v[170:173], v[106:109]
	v_mfma_f32_16x16x32_bf16 v[94:97], v[130:133], v[178:181], v[94:97]
	v_mfma_f32_16x16x32_bf16 v[90:93], v[138:141], v[178:181], v[90:93]
	v_mfma_f32_16x16x32_bf16 v[78:81], v[130:133], v[186:189], v[78:81]
	v_mfma_f32_16x16x32_bf16 v[74:77], v[138:141], v[186:189], v[74:77]
	v_mfma_f32_16x16x32_bf16 v[126:129], v[134:137], v[166:169], v[126:129]
	v_mfma_f32_16x16x32_bf16 v[122:125], v[142:145], v[166:169], v[122:125]
	v_mfma_f32_16x16x32_bf16 v[110:113], v[134:137], v[174:177], v[110:113]
	v_mfma_f32_16x16x32_bf16 v[106:109], v[142:145], v[174:177], v[106:109]
	v_mfma_f32_16x16x32_bf16 v[94:97], v[134:137], v[182:185], v[94:97]
	v_mfma_f32_16x16x32_bf16 v[90:93], v[142:145], v[182:185], v[90:93]
	v_mfma_f32_16x16x32_bf16 v[78:81], v[134:137], v[196:199], v[78:81]
	v_mfma_f32_16x16x32_bf16 v[74:77], v[142:145], v[196:199], v[74:77]
	s_setprio 0
	s_setprio 1
	v_mfma_f32_16x16x32_bf16 v[118:121], v[146:149], v[162:165], v[118:121]
	v_mfma_f32_16x16x32_bf16 v[114:117], v[154:157], v[162:165], v[114:117]
	v_mfma_f32_16x16x32_bf16 v[102:105], v[146:149], v[170:173], v[102:105]
	v_mfma_f32_16x16x32_bf16 v[98:101], v[154:157], v[170:173], v[98:101]
	v_mfma_f32_16x16x32_bf16 v[86:89], v[146:149], v[178:181], v[86:89]
	v_mfma_f32_16x16x32_bf16 v[82:85], v[154:157], v[178:181], v[82:85]
	v_mfma_f32_16x16x32_bf16 v[70:73], v[146:149], v[186:189], v[70:73]
	v_mfma_f32_16x16x32_bf16 v[66:69], v[154:157], v[186:189], v[66:69]
	v_mfma_f32_16x16x32_bf16 v[118:121], v[150:153], v[166:169], v[118:121]
	v_mfma_f32_16x16x32_bf16 v[114:117], v[158:161], v[166:169], v[114:117]
	v_mfma_f32_16x16x32_bf16 v[102:105], v[150:153], v[174:177], v[102:105]
	v_mfma_f32_16x16x32_bf16 v[98:101], v[158:161], v[174:177], v[98:101]
	v_mfma_f32_16x16x32_bf16 v[86:89], v[150:153], v[182:185], v[86:89]
	v_mfma_f32_16x16x32_bf16 v[82:85], v[158:161], v[182:185], v[82:85]
	v_mfma_f32_16x16x32_bf16 v[70:73], v[150:153], v[196:199], v[70:73]
	v_mfma_f32_16x16x32_bf16 v[66:69], v[158:161], v[196:199], v[66:69]
.Lcj1_662:
	s_setprio 0
	s_barrier
	s_and_b64 s[58:59], s[56:57], exec
	s_cselect_b32 s62, 0, s55
	s_and_b64 s[56:57], s[2:3], s[56:57]
	s_and_b64 s[56:57], s[56:57], exec
	s_cselect_b32 s5, s54, s5
	s_cselect_b32 s4, s17, s4
	s_cselect_b32 s1, s53, s1
	s_cselect_b32 s0, s19, s0
	s_lshl_b64 s[56:57], s[62:63], 7
	s_add_u32 s58, s4, s56
	s_addc_u32 s59, s5, s57
	s_mov_b32 m0, s37
	s_add_u32 s60, s4, 0x40000
	ds_read_b128 v[162:165], v217 offset:16384
	ds_read_b128 v[166:169], v217 offset:17408
	ds_read_b128 v[170:173], v217 offset:18432
	ds_read_b128 v[174:177], v217 offset:19456
	ds_read_b128 v[178:181], v217 offset:20480
	ds_read_b128 v[182:185], v217 offset:21504
	ds_read_b128 v[186:189], v217 offset:22528
	ds_read_b128 v[196:199], v217 offset:23552
	global_load_lds_dwordx4 v190, s[58:59]
	s_mov_b32 m0, s38
	s_addc_u32 s61, s5, 0
	global_load_lds_dwordx4 v216, s[58:59]
	s_add_u32 s58, s60, s56
	s_addc_u32 s59, s61, s57
	s_mov_b32 m0, s39
	s_add_u32 s56, s0, s56
	global_load_lds_dwordx4 v190, s[58:59]
	s_mov_b32 m0, s40
	s_addc_u32 s57, s1, s57
	global_load_lds_dwordx4 v216, s[58:59]
	s_mov_b32 m0, s31
	s_nop 0
	global_load_lds_dwordx4 v194, s[56:57]
	s_mov_b32 m0, s41
	s_nop 0
	global_load_lds_dwordx4 v192, s[56:57]
	s_cmp_lg_u32 s100, 0
	s_waitcnt vmcnt(8)
	s_waitcnt lgkmcnt(0)
	s_barrier
	s_setprio 1
	s_cbranch_scc1 .Lcz2_662
	v_mfma_f32_16x16x32_bf16 v[62:65], v[130:133], v[162:165], v[62:65]
	v_mfma_f32_16x16x32_bf16 v[58:61], v[138:141], v[162:165], v[58:61]
	v_mfma_f32_16x16x32_bf16 v[46:49], v[130:133], v[170:173], v[46:49]
	v_mfma_f32_16x16x32_bf16 v[42:45], v[138:141], v[170:173], v[42:45]
	v_mfma_f32_16x16x32_bf16 v[30:33], v[130:133], v[178:181], v[30:33]
	v_mfma_f32_16x16x32_bf16 v[26:29], v[138:141], v[178:181], v[26:29]
	v_mfma_f32_16x16x32_bf16 v[14:17], v[130:133], v[186:189], v[14:17]
	v_mfma_f32_16x16x32_bf16 v[10:13], v[138:141], v[186:189], v[10:13]
	v_mfma_f32_16x16x32_bf16 v[62:65], v[134:137], v[166:169], v[62:65]
	v_mfma_f32_16x16x32_bf16 v[58:61], v[142:145], v[166:169], v[58:61]
	v_mfma_f32_16x16x32_bf16 v[46:49], v[134:137], v[174:177], v[46:49]
	v_mfma_f32_16x16x32_bf16 v[42:45], v[142:145], v[174:177], v[42:45]
	v_mfma_f32_16x16x32_bf16 v[30:33], v[134:137], v[182:185], v[30:33]
	v_mfma_f32_16x16x32_bf16 v[26:29], v[142:145], v[182:185], v[26:29]
	v_mfma_f32_16x16x32_bf16 v[14:17], v[134:137], v[196:199], v[14:17]
	v_mfma_f32_16x16x32_bf16 v[10:13], v[142:145], v[196:199], v[10:13]
	s_setprio 0
	s_setprio 1
	v_mfma_f32_16x16x32_bf16 v[54:57], v[146:149], v[162:165], v[54:57]
	v_mfma_f32_16x16x32_bf16 v[50:53], v[154:157], v[162:165], v[50:53]
	v_mfma_f32_16x16x32_bf16 v[38:41], v[146:149], v[170:173], v[38:41]
	v_mfma_f32_16x16x32_bf16 v[34:37], v[154:157], v[170:173], v[34:37]
	v_mfma_f32_16x16x32_bf16 v[22:25], v[146:149], v[178:181], v[22:25]
	v_mfma_f32_16x16x32_bf16 v[18:21], v[154:157], v[178:181], v[18:21]
	v_mfma_f32_16x16x32_bf16 v[6:9], v[146:149], v[186:189], v[6:9]
	v_mfma_f32_16x16x32_bf16 v[2:5], v[154:157], v[186:189], v[2:5]
	v_mfma_f32_16x16x32_bf16 v[54:57], v[150:153], v[166:169], v[54:57]
	v_mfma_f32_16x16x32_bf16 v[50:53], v[158:161], v[166:169], v[50:53]
	v_mfma_f32_16x16x32_bf16 v[38:41], v[150:153], v[174:177], v[38:41]
	v_mfma_f32_16x16x32_bf16 v[34:37], v[158:161], v[174:177], v[34:37]
	v_mfma_f32_16x16x32_bf16 v[22:25], v[150:153], v[182:185], v[22:25]
	v_mfma_f32_16x16x32_bf16 v[18:21], v[158:161], v[182:185], v[18:21]
	v_mfma_f32_16x16x32_bf16 v[6:9], v[150:153], v[196:199], v[6:9]
	v_mfma_f32_16x16x32_bf16 v[2:5], v[158:161], v[196:199], v[2:5]
.Lcj2_662:
	s_setprio 0
	s_barrier
	v_add_u32_e32 v142, 0x18000, v191
	v_add_u32_e32 v158, 0x1c000, v191
	ds_read_b128 v[130:133], v142
	ds_read_b128 v[134:137], v142 offset:1024
	ds_read_b128 v[138:141], v142 offset:2048
	ds_read_b128 v[142:145], v142 offset:3072
	ds_read_b128 v[146:149], v158
	ds_read_b128 v[150:153], v158 offset:1024
	ds_read_b128 v[154:157], v158 offset:2048
	ds_read_b128 v[158:161], v158 offset:3072
	s_add_u32 s56, s56, 0x40000
	s_addc_u32 s57, s57, 0
	s_mov_b32 m0, s42
	ds_read_b128 v[162:165], v217 offset:32768
	ds_read_b128 v[166:169], v217 offset:33792
	ds_read_b128 v[170:173], v217 offset:34816
	ds_read_b128 v[174:177], v217 offset:35840
	ds_read_b128 v[178:181], v217 offset:36864
	ds_read_b128 v[182:185], v217 offset:37888
	ds_read_b128 v[186:189], v217 offset:38912
	ds_read_b128 v[196:199], v217 offset:39936
	global_load_lds_dwordx4 v194, s[56:57]
	s_mov_b32 m0, s43
	s_nop 0
	global_load_lds_dwordx4 v192, s[56:57]
	s_waitcnt vmcnt(8)
	s_waitcnt lgkmcnt(0)
	s_barrier
	s_setprio 1
	v_mfma_f32_16x16x32_bf16 v[126:129], v[130:133], v[162:165], v[126:129]
	v_mfma_f32_16x16x32_bf16 v[122:125], v[138:141], v[162:165], v[122:125]
	v_mfma_f32_16x16x32_bf16 v[110:113], v[130:133], v[170:173], v[110:113]
	v_mfma_f32_16x16x32_bf16 v[106:109], v[138:141], v[170:173], v[106:109]
	v_mfma_f32_16x16x32_bf16 v[94:97], v[130:133], v[178:181], v[94:97]
	v_mfma_f32_16x16x32_bf16 v[90:93], v[138:141], v[178:181], v[90:93]
	v_mfma_f32_16x16x32_bf16 v[78:81], v[130:133], v[186:189], v[78:81]
	v_mfma_f32_16x16x32_bf16 v[74:77], v[138:141], v[186:189], v[74:77]
	v_mfma_f32_16x16x32_bf16 v[126:129], v[134:137], v[166:169], v[126:129]
	v_mfma_f32_16x16x32_bf16 v[122:125], v[142:145], v[166:169], v[122:125]
	v_mfma_f32_16x16x32_bf16 v[110:113], v[134:137], v[174:177], v[110:113]
	v_mfma_f32_16x16x32_bf16 v[106:109], v[142:145], v[174:177], v[106:109]
	v_mfma_f32_16x16x32_bf16 v[94:97], v[134:137], v[182:185], v[94:97]
	v_mfma_f32_16x16x32_bf16 v[90:93], v[142:145], v[182:185], v[90:93]
	v_mfma_f32_16x16x32_bf16 v[78:81], v[134:137], v[196:199], v[78:81]
	v_mfma_f32_16x16x32_bf16 v[74:77], v[142:145], v[196:199], v[74:77]
	s_setprio 0
	s_setprio 1
	v_mfma_f32_16x16x32_bf16 v[118:121], v[146:149], v[162:165], v[118:121]
	v_mfma_f32_16x16x32_bf16 v[114:117], v[154:157], v[162:165], v[114:117]
	v_mfma_f32_16x16x32_bf16 v[102:105], v[146:149], v[170:173], v[102:105]
	v_mfma_f32_16x16x32_bf16 v[98:101], v[154:157], v[170:173], v[98:101]
	v_mfma_f32_16x16x32_bf16 v[86:89], v[146:149], v[178:181], v[86:89]
	v_mfma_f32_16x16x32_bf16 v[82:85], v[154:157], v[178:181], v[82:85]
	v_mfma_f32_16x16x32_bf16 v[70:73], v[146:149], v[186:189], v[70:73]
	v_mfma_f32_16x16x32_bf16 v[66:69], v[154:157], v[186:189], v[66:69]
	v_mfma_f32_16x16x32_bf16 v[118:121], v[150:153], v[166:169], v[118:121]
	v_mfma_f32_16x16x32_bf16 v[114:117], v[158:161], v[166:169], v[114:117]
	v_mfma_f32_16x16x32_bf16 v[102:105], v[150:153], v[174:177], v[102:105]
	v_mfma_f32_16x16x32_bf16 v[98:101], v[158:161], v[174:177], v[98:101]
	v_mfma_f32_16x16x32_bf16 v[86:89], v[150:153], v[182:185], v[86:89]
	v_mfma_f32_16x16x32_bf16 v[82:85], v[158:161], v[182:185], v[82:85]
	v_mfma_f32_16x16x32_bf16 v[70:73], v[150:153], v[196:199], v[70:73]
	v_mfma_f32_16x16x32_bf16 v[66:69], v[158:161], v[196:199], v[66:69]
	s_setprio 0
	s_barrier
	s_or_b32 s62, s62, 1
	s_lshl_b64 s[56:57], s[62:63], 7
	s_add_u32 s58, s4, s56
	s_mov_b32 m0, s45
	s_addc_u32 s59, s5, s57
	ds_read_b128 v[162:165], v217 offset:49152
	ds_read_b128 v[166:169], v217 offset:50176
	ds_read_b128 v[170:173], v217 offset:51200
	ds_read_b128 v[174:177], v217 offset:52224
	ds_read_b128 v[178:181], v217 offset:53248
	ds_read_b128 v[182:185], v217 offset:54272
	ds_read_b128 v[186:189], v217 offset:55296
	ds_read_b128 v[196:199], v217 offset:56320
	global_load_lds_dwordx4 v190, s[58:59]
	s_mov_b32 m0, s46
	s_nop 0
	global_load_lds_dwordx4 v216, s[58:59]
	s_add_u32 s58, s60, s56
	s_addc_u32 s59, s61, s57
	s_mov_b32 m0, s49
	s_add_u32 s56, s0, s56
	global_load_lds_dwordx4 v190, s[58:59]
	s_mov_b32 m0, s50
	s_addc_u32 s57, s1, s57
	global_load_lds_dwordx4 v216, s[58:59]
	s_mov_b32 m0, s47
	s_nop 0
	global_load_lds_dwordx4 v194, s[56:57]
	s_mov_b32 m0, s48
	s_nop 0
	global_load_lds_dwordx4 v192, s[56:57]
	s_waitcnt vmcnt(8)
	s_waitcnt lgkmcnt(0)
	s_barrier
	s_setprio 1
	v_mfma_f32_16x16x32_bf16 v[62:65], v[130:133], v[162:165], v[62:65]
	v_mfma_f32_16x16x32_bf16 v[58:61], v[138:141], v[162:165], v[58:61]
	v_mfma_f32_16x16x32_bf16 v[46:49], v[130:133], v[170:173], v[46:49]
	v_mfma_f32_16x16x32_bf16 v[42:45], v[138:141], v[170:173], v[42:45]
	v_mfma_f32_16x16x32_bf16 v[30:33], v[130:133], v[178:181], v[30:33]
	v_mfma_f32_16x16x32_bf16 v[26:29], v[138:141], v[178:181], v[26:29]
	v_mfma_f32_16x16x32_bf16 v[14:17], v[130:133], v[186:189], v[14:17]
	v_mfma_f32_16x16x32_bf16 v[10:13], v[138:141], v[186:189], v[10:13]
	v_mfma_f32_16x16x32_bf16 v[62:65], v[134:137], v[166:169], v[62:65]
	v_mfma_f32_16x16x32_bf16 v[58:61], v[142:145], v[166:169], v[58:61]
	v_mfma_f32_16x16x32_bf16 v[46:49], v[134:137], v[174:177], v[46:49]
	v_mfma_f32_16x16x32_bf16 v[42:45], v[142:145], v[174:177], v[42:45]
	v_mfma_f32_16x16x32_bf16 v[30:33], v[134:137], v[182:185], v[30:33]
	v_mfma_f32_16x16x32_bf16 v[26:29], v[142:145], v[182:185], v[26:29]
	v_mfma_f32_16x16x32_bf16 v[14:17], v[134:137], v[196:199], v[14:17]
	v_mfma_f32_16x16x32_bf16 v[10:13], v[142:145], v[196:199], v[10:13]
	s_setprio 0
	s_setprio 1
	v_mfma_f32_16x16x32_bf16 v[54:57], v[146:149], v[162:165], v[54:57]
	v_mfma_f32_16x16x32_bf16 v[50:53], v[154:157], v[162:165], v[50:53]
	v_mfma_f32_16x16x32_bf16 v[38:41], v[146:149], v[170:173], v[38:41]
	v_mfma_f32_16x16x32_bf16 v[34:37], v[154:157], v[170:173], v[34:37]
	v_mfma_f32_16x16x32_bf16 v[22:25], v[146:149], v[178:181], v[22:25]
	v_mfma_f32_16x16x32_bf16 v[18:21], v[154:157], v[178:181], v[18:21]
	v_mfma_f32_16x16x32_bf16 v[6:9], v[146:149], v[186:189], v[6:9]
	v_mfma_f32_16x16x32_bf16 v[2:5], v[154:157], v[186:189], v[2:5]
	v_mfma_f32_16x16x32_bf16 v[54:57], v[150:153], v[166:169], v[54:57]
	v_mfma_f32_16x16x32_bf16 v[50:53], v[158:161], v[166:169], v[50:53]
	v_mfma_f32_16x16x32_bf16 v[38:41], v[150:153], v[174:177], v[38:41]
	v_mfma_f32_16x16x32_bf16 v[34:37], v[158:161], v[174:177], v[34:37]
	v_mfma_f32_16x16x32_bf16 v[22:25], v[150:153], v[182:185], v[22:25]
	v_mfma_f32_16x16x32_bf16 v[18:21], v[158:161], v[182:185], v[18:21]
	v_mfma_f32_16x16x32_bf16 v[6:9], v[150:153], v[196:199], v[6:9]
	v_mfma_f32_16x16x32_bf16 v[2:5], v[158:161], v[196:199], v[2:5]
	s_setprio 0
	s_barrier
	s_add_i32 s56, s55, 2
	s_add_u32 s22, s22, 0x100
	s_addc_u32 s23, s23, 0
	s_cmp_ge_i32 s55, s52
	s_mov_b32 s55, s56
	s_cbranch_scc0 .LBB0_662
	s_branch .Lcsk_662

.LBB0_961:
	v_add_u32_e32 v2, 0x10000, v167
	v_add_u32_e32 v14, 0x14000, v167
	ds_read_b128 v[18:21], v2
	ds_read_b128 v[22:25], v2 offset:1024
	ds_read_b128 v[26:29], v2 offset:2048
	ds_read_b128 v[30:33], v2 offset:3072
	ds_read_b128 v[2:5], v14
	ds_read_b128 v[6:9], v14 offset:1024
	ds_read_b128 v[10:13], v14 offset:2048
	ds_read_b128 v[14:17], v14 offset:3072
	s_add_i32 m0, s41, 0xc000
	s_add_i32 s28, s41, 0xe000
	s_cmp_lg_u32 s19, s60
	s_cselect_b64 s[30:31], -1, 0
	v_lshl_add_u64 v[188:189], s[20:21], 0, v[194:195]
	v_lshl_add_u64 v[188:189], v[188:189], 0, s[26:27]
	v_mov_b32_e32 v169, v195
	ds_read_b128 v[180:183], v170
	ds_read_b128 v[184:187], v170 offset:1024
	ds_read_b128 v[216:219], v170 offset:2048
	ds_read_b128 v[220:223], v170 offset:3072
	ds_read_b128 v[224:227], v170 offset:4096
	ds_read_b128 v[228:231], v170 offset:5120
	ds_read_b128 v[196:199], v170 offset:6144
	ds_read_b128 v[200:203], v170 offset:7168
	global_load_lds_dwordx4 v[188:189], off
	v_lshl_add_u64 v[188:189], s[20:21], 0, v[168:169]
	v_lshl_add_u64 v[188:189], v[188:189], 0, s[26:27]
	s_mov_b32 m0, s28
	s_nop 0
	global_load_lds_dwordx4 v[188:189], off
	s_cmp_lg_u32 s100, 0
	s_waitcnt vmcnt(8)
	s_waitcnt lgkmcnt(0)
	s_barrier
	s_setprio 1
	s_cbranch_scc1 .Lcz1_961
	v_mfma_f32_16x16x128_f8f6f4 v[146:149], v[18:25], v[180:187], v[146:149]
	v_mfma_f32_16x16x128_f8f6f4 v[158:161], v[26:33], v[180:187], v[158:161]
	v_mfma_f32_16x16x128_f8f6f4 v[142:145], v[18:25], v[216:223], v[142:145]
	v_mfma_f32_16x16x128_f8f6f4 v[138:141], v[26:33], v[216:223], v[138:141]
	v_mfma_f32_16x16x128_f8f6f4 v[126:129], v[18:25], v[224:231], v[126:129]
	v_mfma_f32_16x16x128_f8f6f4 v[122:125], v[26:33], v[224:231], v[122:125]
	v_mfma_f32_16x16x128_f8f6f4 v[110:113], v[18:25], v[196:203], v[110:113]
	v_mfma_f32_16x16x128_f8f6f4 v[106:109], v[26:33], v[196:203], v[106:109]
	s_setprio 0
	s_setprio 1
	v_mfma_f32_16x16x128_f8f6f4 v[154:157], v[2:9], v[180:187], v[154:157]
	v_mfma_f32_16x16x128_f8f6f4 v[150:153], v[10:17], v[180:187], v[150:153]
	v_mfma_f32_16x16x128_f8f6f4 v[134:137], v[2:9], v[216:223], v[134:137]
	v_mfma_f32_16x16x128_f8f6f4 v[130:133], v[10:17], v[216:223], v[130:133]
	v_mfma_f32_16x16x128_f8f6f4 v[118:121], v[2:9], v[224:231], v[118:121]
	v_mfma_f32_16x16x128_f8f6f4 v[114:117], v[10:17], v[224:231], v[114:117]
	v_mfma_f32_16x16x128_f8f6f4 v[102:105], v[2:9], v[196:203], v[102:105]
	v_mfma_f32_16x16x128_f8f6f4 v[98:101], v[10:17], v[196:203], v[98:101]

.LBB0_963:
	s_ashr_i32 s29, s28, 31
	s_lshl_b64 s[28:29], s[28:29], 7
	s_add_u32 s30, s12, s28
	s_mov_b32 m0, s42
	s_addc_u32 s31, s13, s29
	ds_read_b128 v[180:183], v170 offset:16384
	ds_read_b128 v[184:187], v170 offset:17408
	ds_read_b128 v[196:199], v170 offset:18432
	ds_read_b128 v[200:203], v170 offset:19456
	ds_read_b128 v[216:219], v170 offset:20480
	ds_read_b128 v[220:223], v170 offset:21504
	ds_read_b128 v[224:227], v170 offset:22528
	ds_read_b128 v[228:231], v170 offset:23552
	global_load_lds_dwordx4 v171, s[30:31]
	s_mov_b32 m0, s43
	s_nop 0
	global_load_lds_dwordx4 v162, s[30:31]
	s_add_u32 s30, s12, 0x20000
	s_addc_u32 s31, s13, 0
	s_add_u32 s66, s30, s28
	s_addc_u32 s67, s31, s29
	s_mov_b32 m0, s44
	s_nop 0
	global_load_lds_dwordx4 v171, s[66:67]
	s_mov_b32 m0, s45
	s_nop 0
	global_load_lds_dwordx4 v162, s[66:67]
	s_add_u32 s66, s20, s28
	s_addc_u32 s67, s21, s29
	s_mov_b32 m0, s41
	s_nop 0
	global_load_lds_dwordx4 v164, s[66:67]
	s_mov_b32 m0, s46
	s_nop 0
	global_load_lds_dwordx4 v166, s[66:67]
	s_cmp_lg_u32 s100, 0
	s_waitcnt vmcnt(8)
	s_waitcnt lgkmcnt(0)
	s_barrier
	s_setprio 1
	s_cbranch_scc1 .Lcz2_961
	v_mfma_f32_16x16x128_f8f6f4 v[94:97], v[18:25], v[180:187], v[94:97]
	v_mfma_f32_16x16x128_f8f6f4 v[90:93], v[26:33], v[180:187], v[90:93]
	v_mfma_f32_16x16x128_f8f6f4 v[78:81], v[18:25], v[196:203], v[78:81]
	v_mfma_f32_16x16x128_f8f6f4 v[74:77], v[26:33], v[196:203], v[74:77]
	v_mfma_f32_16x16x128_f8f6f4 v[188:191], v[18:25], v[216:223], v[62:65]
	v_mfma_f32_16x16x128_f8f6f4 v[248:251], v[26:33], v[216:223], v[58:61]
	v_mfma_f32_16x16x128_f8f6f4 v[242:245], v[18:25], v[224:231], v[46:49]
	v_mfma_f32_16x16x128_f8f6f4 v[208:211], v[26:33], v[224:231], v[42:45]
	s_setprio 0
	s_setprio 1
	v_mfma_f32_16x16x128_f8f6f4 v[86:89], v[2:9], v[180:187], v[86:89]
	v_mfma_f32_16x16x128_f8f6f4 v[82:85], v[10:17], v[180:187], v[82:85]
	v_mfma_f32_16x16x128_f8f6f4 v[70:73], v[2:9], v[196:203], v[70:73]
	v_mfma_f32_16x16x128_f8f6f4 v[66:69], v[10:17], v[196:203], v[66:69]
	v_mfma_f32_16x16x128_f8f6f4 v[212:215], v[2:9], v[216:223], v[54:57]
	v_mfma_f32_16x16x128_f8f6f4 v[216:219], v[10:17], v[216:223], v[50:53]
	v_mfma_f32_16x16x128_f8f6f4 v[220:223], v[2:9], v[224:231], v[38:41]
	v_mfma_f32_16x16x128_f8f6f4 v[224:227], v[10:17], v[224:231], v[34:37]
.Lcj2_961:
	s_setprio 0
	s_barrier
	v_add_u32_e32 v14, 0x18000, v167
	v_add_u32_e32 v30, 0x1c000, v167
	ds_read_b128 v[2:5], v14
	ds_read_b128 v[6:9], v14 offset:1024
	ds_read_b128 v[10:13], v14 offset:2048
	ds_read_b128 v[14:17], v14 offset:3072
	ds_read_b128 v[18:21], v30
	ds_read_b128 v[22:25], v30 offset:1024
	ds_read_b128 v[26:29], v30 offset:2048
	ds_read_b128 v[30:33], v30 offset:3072
	s_mov_b32 m0, s47
	v_lshl_add_u64 v[180:181], s[66:67], 0, v[194:195]
	ds_read_b128 v[34:37], v170 offset:32768
	ds_read_b128 v[38:41], v170 offset:33792
	ds_read_b128 v[42:45], v170 offset:34816
	ds_read_b128 v[46:49], v170 offset:35840
	ds_read_b128 v[50:53], v170 offset:36864
	ds_read_b128 v[54:57], v170 offset:37888
	ds_read_b128 v[58:61], v170 offset:38912
	ds_read_b128 v[62:65], v170 offset:39936
	global_load_lds_dwordx4 v[180:181], off
	v_lshl_add_u64 v[180:181], s[66:67], 0, v[168:169]
	s_mov_b32 m0, s48
	s_nop 0
	global_load_lds_dwordx4 v[180:181], off
	s_waitcnt vmcnt(8)
	s_waitcnt lgkmcnt(0)
	s_barrier
	s_setprio 1
	v_mfma_f32_16x16x128_f8f6f4 v[146:149], v[2:9], v[34:41], v[146:149]
	v_mfma_f32_16x16x128_f8f6f4 v[158:161], v[10:17], v[34:41], v[158:161]
	v_mfma_f32_16x16x128_f8f6f4 v[142:145], v[2:9], v[42:49], v[142:145]
	v_mfma_f32_16x16x128_f8f6f4 v[138:141], v[10:17], v[42:49], v[138:141]
	v_mfma_f32_16x16x128_f8f6f4 v[126:129], v[2:9], v[50:57], v[126:129]
	v_mfma_f32_16x16x128_f8f6f4 v[122:125], v[10:17], v[50:57], v[122:125]
	v_mfma_f32_16x16x128_f8f6f4 v[110:113], v[2:9], v[58:65], v[110:113]
	v_mfma_f32_16x16x128_f8f6f4 v[106:109], v[10:17], v[58:65], v[106:109]
	s_setprio 0
	s_setprio 1
	v_mfma_f32_16x16x128_f8f6f4 v[154:157], v[18:25], v[34:41], v[154:157]
	v_mfma_f32_16x16x128_f8f6f4 v[150:153], v[26:33], v[34:41], v[150:153]
	v_mfma_f32_16x16x128_f8f6f4 v[134:137], v[18:25], v[42:49], v[134:137]
	v_mfma_f32_16x16x128_f8f6f4 v[130:133], v[26:33], v[42:49], v[130:133]
	v_mfma_f32_16x16x128_f8f6f4 v[118:121], v[18:25], v[50:57], v[118:121]
	v_mfma_f32_16x16x128_f8f6f4 v[114:117], v[26:33], v[50:57], v[114:117]
	v_mfma_f32_16x16x128_f8f6f4 v[102:105], v[18:25], v[58:65], v[102:105]
	v_mfma_f32_16x16x128_f8f6f4 v[98:101], v[26:33], v[58:65], v[98:101]
	s_setprio 0
	s_barrier
	s_add_u32 s61, s28, 0x80
	s_addc_u32 s62, s29, 0
	s_add_u32 s28, s12, s61
	s_mov_b32 m0, s49
	s_addc_u32 s29, s13, s62
	ds_read_b128 v[34:37], v170 offset:49152
	ds_read_b128 v[38:41], v170 offset:50176
	ds_read_b128 v[50:53], v170 offset:51200
	ds_read_b128 v[54:57], v170 offset:52224
	ds_read_b128 v[180:183], v170 offset:53248
	ds_read_b128 v[184:187], v170 offset:54272
	ds_read_b128 v[196:199], v170 offset:55296
	ds_read_b128 v[200:203], v170 offset:56320
	global_load_lds_dwordx4 v171, s[28:29]
	s_mov_b32 m0, s50
	s_nop 0
	global_load_lds_dwordx4 v162, s[28:29]
	s_add_u32 s28, s30, s61
	s_addc_u32 s29, s31, s62
	s_mov_b32 m0, s53
	s_nop 0
	global_load_lds_dwordx4 v171, s[28:29]
	s_mov_b32 m0, s54
	s_nop 0
	global_load_lds_dwordx4 v162, s[28:29]
	s_add_u32 s28, s20, s61
	s_addc_u32 s29, s21, s62
	s_mov_b32 m0, s51
	s_nop 0
	global_load_lds_dwordx4 v164, s[28:29]
	s_mov_b32 m0, s52
	s_nop 0
	global_load_lds_dwordx4 v166, s[28:29]
	s_waitcnt vmcnt(8)
	s_waitcnt lgkmcnt(0)
	s_barrier
	s_setprio 1
	v_mfma_f32_16x16x128_f8f6f4 v[94:97], v[2:9], v[34:41], v[94:97]
	v_mfma_f32_16x16x128_f8f6f4 v[90:93], v[10:17], v[34:41], v[90:93]
	v_mfma_f32_16x16x128_f8f6f4 v[78:81], v[2:9], v[50:57], v[78:81]
	v_mfma_f32_16x16x128_f8f6f4 v[74:77], v[10:17], v[50:57], v[74:77]
	v_mfma_f32_16x16x128_f8f6f4 v[62:65], v[2:9], v[180:187], v[188:191]
	v_mfma_f32_16x16x128_f8f6f4 v[58:61], v[10:17], v[180:187], v[248:251]
	v_mfma_f32_16x16x128_f8f6f4 v[46:49], v[2:9], v[196:203], v[242:245]
	v_mfma_f32_16x16x128_f8f6f4 v[42:45], v[10:17], v[196:203], v[208:211]
	s_setprio 0
	s_setprio 1
	v_mfma_f32_16x16x128_f8f6f4 v[86:89], v[18:25], v[34:41], v[86:89]
	v_mfma_f32_16x16x128_f8f6f4 v[82:85], v[26:33], v[34:41], v[82:85]
	v_mfma_f32_16x16x128_f8f6f4 v[70:73], v[18:25], v[50:57], v[70:73]
	v_mfma_f32_16x16x128_f8f6f4 v[66:69], v[26:33], v[50:57], v[66:69]
	v_mfma_f32_16x16x128_f8f6f4 v[54:57], v[18:25], v[180:187], v[212:215]
	v_mfma_f32_16x16x128_f8f6f4 v[50:53], v[26:33], v[180:187], v[216:219]
	v_mfma_f32_16x16x128_f8f6f4 v[38:41], v[18:25], v[196:203], v[220:223]
	v_mfma_f32_16x16x128_f8f6f4 v[34:37], v[26:33], v[196:203], v[224:227]
	s_setprio 0
	s_barrier
	s_add_i32 s28, s60, 2
	s_add_u32 s26, s26, 0x100
	s_addc_u32 s27, s27, 0
	s_cmp_ge_i32 s60, s19
	s_cbranch_scc1 .LBB0_966
	s_mov_b32 s60, s28
	s_branch .LBB0_961

.LBB0_1048:
	v_add_u32_e32 v66, 0x10000, v131
	ds_read_b128 v[136:139], v66
	ds_read_b128 v[140:143], v66 offset:1024
	ds_read_b128 v[144:147], v66 offset:2048
	ds_read_b128 v[148:151], v66 offset:3072
	v_add_u32_e32 v66, 0x14000, v131
	ds_read_b128 v[152:155], v66
	ds_read_b128 v[156:159], v66 offset:1024
	ds_read_b128 v[160:163], v66 offset:2048
	ds_read_b128 v[164:167], v66 offset:3072
	s_add_i32 m0, s31, 0xc000
	s_add_i32 s57, s31, 0xe000
	s_cmp_eq_u32 s55, s56
	s_cselect_b64 s[22:23], -1, 0
	v_lshl_add_u64 v[66:67], s[0:1], 0, v[194:195]
	v_lshl_add_u64 v[66:67], v[66:67], 0, s[20:21]
	v_mov_b32_e32 v133, v195
	ds_read_b128 v[168:171], v135
	ds_read_b128 v[172:175], v135 offset:1024
	ds_read_b128 v[176:179], v135 offset:2048
	ds_read_b128 v[180:183], v135 offset:3072
	ds_read_b128 v[184:187], v135 offset:4096
	ds_read_b128 v[188:191], v135 offset:5120
	ds_read_b128 v[196:199], v135 offset:6144
	ds_read_b128 v[200:203], v135 offset:7168
	global_load_lds_dwordx4 v[66:67], off
	v_lshl_add_u64 v[66:67], s[0:1], 0, v[132:133]
	v_lshl_add_u64 v[66:67], v[66:67], 0, s[20:21]
	s_mov_b32 m0, s57
	s_nop 0
	global_load_lds_dwordx4 v[66:67], off
	s_cmp_lg_u32 s100, 0
	s_waitcnt vmcnt(8)
	s_waitcnt lgkmcnt(0)
	s_barrier
	s_setprio 1
	s_cbranch_scc1 .Lcz1_1048
	v_mfma_f32_16x16x128_f8f6f4 v[126:129], v[136:143], v[168:175], v[126:129]
	v_mfma_f32_16x16x128_f8f6f4 v[122:125], v[144:151], v[168:175], v[122:125]
	v_mfma_f32_16x16x128_f8f6f4 v[110:113], v[136:143], v[176:183], v[110:113]
	v_mfma_f32_16x16x128_f8f6f4 v[106:109], v[144:151], v[176:183], v[106:109]
	v_mfma_f32_16x16x128_f8f6f4 v[208:211], v[136:143], v[184:191], v[94:97]
	v_mfma_f32_16x16x128_f8f6f4 v[212:215], v[144:151], v[184:191], v[90:93]
	v_mfma_f32_16x16x128_f8f6f4 v[216:219], v[136:143], v[196:203], v[78:81]
	v_mfma_f32_16x16x128_f8f6f4 v[220:223], v[144:151], v[196:203], v[74:77]
	s_setprio 0
	s_setprio 1
	v_mfma_f32_16x16x128_f8f6f4 v[118:121], v[152:159], v[168:175], v[118:121]
	v_mfma_f32_16x16x128_f8f6f4 v[114:117], v[160:167], v[168:175], v[114:117]
	v_mfma_f32_16x16x128_f8f6f4 v[102:105], v[152:159], v[176:183], v[102:105]
	v_mfma_f32_16x16x128_f8f6f4 v[98:101], v[160:167], v[176:183], v[98:101]
	v_mfma_f32_16x16x128_f8f6f4 v[168:171], v[152:159], v[184:191], v[86:89]
	v_mfma_f32_16x16x128_f8f6f4 v[172:175], v[160:167], v[184:191], v[82:85]
	v_mfma_f32_16x16x128_f8f6f4 v[176:179], v[152:159], v[196:203], v[70:73]
	v_mfma_f32_16x16x128_f8f6f4 v[180:183], v[160:167], v[196:203], v[10:13]
.Lcj1_1048:
	s_setprio 0
	s_barrier
	s_and_b64 s[58:59], s[22:23], exec
	s_cselect_b32 s62, 0, s56
	s_and_b64 s[22:23], s[4:5], s[22:23]
	s_and_b64 s[22:23], s[22:23], exec
	s_cselect_b32 s7, s19, s7
	s_cselect_b32 s6, s18, s6
	s_cselect_b32 s1, s17, s1
	s_cselect_b32 s0, s16, s0
	s_lshl_b64 s[58:59], s[62:63], 7
	s_add_u32 s22, s6, s58
	s_mov_b32 m0, s36
	s_addc_u32 s23, s7, s59
	ds_read_b128 v[66:69], v135 offset:16384
	ds_read_b128 v[70:73], v135 offset:17408
	ds_read_b128 v[74:77], v135 offset:18432
	ds_read_b128 v[78:81], v135 offset:19456
	ds_read_b128 v[82:85], v135 offset:20480
	ds_read_b128 v[86:89], v135 offset:21504
	ds_read_b128 v[90:93], v135 offset:22528
	ds_read_b128 v[94:97], v135 offset:23552
	global_load_lds_dwordx4 v130, s[22:23]
	s_mov_b32 m0, s37
	s_nop 0
	global_load_lds_dwordx4 v134, s[22:23]
	s_add_u32 s22, s6, 0x58000
	s_addc_u32 s23, s7, 0
	s_add_u32 s60, s22, s58
	s_addc_u32 s61, s23, s59
	s_mov_b32 m0, s38
	s_add_u32 s58, s0, s58
	global_load_lds_dwordx4 v130, s[60:61]
	s_mov_b32 m0, s39
	s_addc_u32 s59, s1, s59
	global_load_lds_dwordx4 v134, s[60:61]
	s_mov_b32 m0, s31
	s_nop 0
	global_load_lds_dwordx4 v194, s[58:59]
	s_mov_b32 m0, s40
	s_nop 0
	global_load_lds_dwordx4 v132, s[58:59]
	s_cmp_lg_u32 s100, 0
	s_waitcnt vmcnt(8)
	s_waitcnt lgkmcnt(0)
	s_barrier
	s_setprio 1
	s_cbranch_scc1 .Lcz2_1048
	v_mfma_f32_16x16x128_f8f6f4 v[62:65], v[136:143], v[66:73], v[62:65]
	v_mfma_f32_16x16x128_f8f6f4 v[58:61], v[144:151], v[66:73], v[58:61]
	v_mfma_f32_16x16x128_f8f6f4 v[228:231], v[144:151], v[90:97], v[228:231]
	v_mfma_f32_16x16x128_f8f6f4 v[184:187], v[136:143], v[74:81], v[46:49]
	v_mfma_f32_16x16x128_f8f6f4 v[188:191], v[144:151], v[74:81], v[42:45]
	v_mfma_f32_16x16x128_f8f6f4 v[196:199], v[136:143], v[82:89], v[30:33]
	v_mfma_f32_16x16x128_f8f6f4 v[200:203], v[144:151], v[82:89], v[26:29]
	v_mfma_f32_16x16x128_f8f6f4 v[224:227], v[136:143], v[90:97], v[14:17]
	s_setprio 0
	s_setprio 1
	v_mfma_f32_16x16x128_f8f6f4 v[54:57], v[152:159], v[66:73], v[54:57]
	v_mfma_f32_16x16x128_f8f6f4 v[50:53], v[160:167], v[66:73], v[50:53]
	v_mfma_f32_16x16x128_f8f6f4 v[242:245], v[152:159], v[74:81], v[38:41]
	v_mfma_f32_16x16x128_f8f6f4 v[248:251], v[160:167], v[74:81], v[34:37]
	v_mfma_f32_16x16x128_f8f6f4 v[232:235], v[152:159], v[82:89], v[22:25]
	v_mfma_f32_16x16x128_f8f6f4 v[238:241], v[160:167], v[82:89], v[18:21]
	v_mfma_f32_16x16x128_f8f6f4 v[204:207], v[152:159], v[90:97], v[6:9]
	v_mfma_f32_16x16x128_f8f6f4 v[66:69], v[160:167], v[90:97], v[2:5]
.Lcj2_1048:
	s_setprio 0
	s_barrier
	v_add_u32_e32 v10, 0x18000, v131
	s_nop 3
	ds_read_b128 v[2:5], v10
	ds_read_b128 v[6:9], v10 offset:1024
	ds_read_b128 v[18:21], v10 offset:2048
	ds_read_b128 v[22:25], v10 offset:3072
	v_add_u32_e32 v10, 0x1c000, v131
	ds_read_b128 v[136:139], v10
	ds_read_b128 v[140:143], v10 offset:1024
	ds_read_b128 v[144:147], v10 offset:2048
	ds_read_b128 v[148:151], v10 offset:3072
	s_add_u32 s58, s58, 0x58000
	s_addc_u32 s59, s59, 0
	s_mov_b32 m0, s41
	ds_read_b128 v[10:13], v135 offset:32768
	ds_read_b128 v[14:17], v135 offset:33792
	ds_read_b128 v[26:29], v135 offset:34816
	ds_read_b128 v[30:33], v135 offset:35840
	ds_read_b128 v[34:37], v135 offset:36864
	ds_read_b128 v[38:41], v135 offset:37888
	ds_read_b128 v[42:45], v135 offset:38912
	ds_read_b128 v[46:49], v135 offset:39936
	global_load_lds_dwordx4 v194, s[58:59]
	s_mov_b32 m0, s42
	s_nop 0
	global_load_lds_dwordx4 v132, s[58:59]
	s_waitcnt vmcnt(8)
	s_waitcnt lgkmcnt(0)
	s_barrier
	s_setprio 1
	v_mfma_f32_16x16x128_f8f6f4 v[126:129], v[2:9], v[10:17], v[126:129]
	v_mfma_f32_16x16x128_f8f6f4 v[122:125], v[18:25], v[10:17], v[122:125]
	v_mfma_f32_16x16x128_f8f6f4 v[110:113], v[2:9], v[26:33], v[110:113]
	v_mfma_f32_16x16x128_f8f6f4 v[106:109], v[18:25], v[26:33], v[106:109]
	v_mfma_f32_16x16x128_f8f6f4 v[94:97], v[2:9], v[34:41], v[208:211]
	v_mfma_f32_16x16x128_f8f6f4 v[90:93], v[18:25], v[34:41], v[212:215]
	v_mfma_f32_16x16x128_f8f6f4 v[78:81], v[2:9], v[42:49], v[216:219]
	v_mfma_f32_16x16x128_f8f6f4 v[74:77], v[18:25], v[42:49], v[220:223]
	s_setprio 0
	s_setprio 1
	v_mfma_f32_16x16x128_f8f6f4 v[118:121], v[136:143], v[10:17], v[118:121]
	v_mfma_f32_16x16x128_f8f6f4 v[114:117], v[144:151], v[10:17], v[114:117]
	v_mfma_f32_16x16x128_f8f6f4 v[102:105], v[136:143], v[26:33], v[102:105]
	v_mfma_f32_16x16x128_f8f6f4 v[98:101], v[144:151], v[26:33], v[98:101]
	v_mfma_f32_16x16x128_f8f6f4 v[86:89], v[136:143], v[34:41], v[168:171]
	v_mfma_f32_16x16x128_f8f6f4 v[82:85], v[144:151], v[34:41], v[172:175]
	v_mfma_f32_16x16x128_f8f6f4 v[70:73], v[136:143], v[42:49], v[176:179]
	v_mfma_f32_16x16x128_f8f6f4 v[10:13], v[144:151], v[42:49], v[180:183]
	s_setprio 0
	s_barrier
	s_or_b32 s62, s62, 1
	s_lshl_b64 s[58:59], s[62:63], 7
	s_add_u32 s60, s6, s58
	s_mov_b32 m0, s43
	s_addc_u32 s61, s7, s59
	ds_read_b128 v[34:37], v135 offset:49152
	ds_read_b128 v[38:41], v135 offset:50176
	ds_read_b128 v[152:155], v135 offset:51200
	ds_read_b128 v[156:159], v135 offset:52224
	ds_read_b128 v[160:163], v135 offset:53248
	ds_read_b128 v[164:167], v135 offset:54272
	ds_read_b128 v[168:171], v135 offset:55296
	ds_read_b128 v[172:175], v135 offset:56320
	global_load_lds_dwordx4 v130, s[60:61]
	s_mov_b32 m0, s44
	s_add_u32 s22, s22, s58
	global_load_lds_dwordx4 v134, s[60:61]
	s_addc_u32 s23, s23, s59
	s_mov_b32 m0, s47
	s_nop 0
	global_load_lds_dwordx4 v130, s[22:23]
	s_mov_b32 m0, s48
	s_nop 0
	global_load_lds_dwordx4 v134, s[22:23]
	s_add_u32 s22, s0, s58
	s_addc_u32 s23, s1, s59
	s_mov_b32 m0, s45
	s_nop 0
	global_load_lds_dwordx4 v194, s[22:23]
	s_mov_b32 m0, s46
	s_nop 0
	global_load_lds_dwordx4 v132, s[22:23]
	s_waitcnt vmcnt(8)
	s_waitcnt lgkmcnt(0)
	s_barrier
	s_setprio 1
	v_mfma_f32_16x16x128_f8f6f4 v[62:65], v[2:9], v[34:41], v[62:65]
	v_mfma_f32_16x16x128_f8f6f4 v[58:61], v[18:25], v[34:41], v[58:61]
	v_mfma_f32_16x16x128_f8f6f4 v[46:49], v[2:9], v[152:159], v[184:187]
	v_mfma_f32_16x16x128_f8f6f4 v[42:45], v[18:25], v[152:159], v[188:191]
	v_mfma_f32_16x16x128_f8f6f4 v[30:33], v[2:9], v[160:167], v[196:199]
	v_mfma_f32_16x16x128_f8f6f4 v[26:29], v[18:25], v[160:167], v[200:203]
	v_mfma_f32_16x16x128_f8f6f4 v[14:17], v[2:9], v[168:175], v[224:227]
	v_mfma_f32_16x16x128_f8f6f4 v[228:231], v[18:25], v[168:175], v[228:231]
	s_setprio 0
	s_setprio 1
	v_mfma_f32_16x16x128_f8f6f4 v[54:57], v[136:143], v[34:41], v[54:57]
	v_mfma_f32_16x16x128_f8f6f4 v[50:53], v[144:151], v[34:41], v[50:53]
	v_mfma_f32_16x16x128_f8f6f4 v[38:41], v[136:143], v[152:159], v[242:245]
	v_mfma_f32_16x16x128_f8f6f4 v[34:37], v[144:151], v[152:159], v[248:251]
	v_mfma_f32_16x16x128_f8f6f4 v[22:25], v[136:143], v[160:167], v[232:235]
	v_mfma_f32_16x16x128_f8f6f4 v[18:21], v[144:151], v[160:167], v[238:241]
	v_mfma_f32_16x16x128_f8f6f4 v[6:9], v[136:143], v[168:175], v[204:207]
	v_mfma_f32_16x16x128_f8f6f4 v[2:5], v[144:151], v[168:175], v[66:69]
	s_setprio 0
	s_barrier
	s_add_i32 s22, s56, 2
	s_add_u32 s20, s20, 0x100
	s_addc_u32 s21, s21, 0
	s_cmp_ge_i32 s56, s55
	s_mov_b32 s56, s22
	s_cbranch_scc0 .LBB0_1048
	s_branch .Lcsk_1048
